# adds: GEMM K-loops (in-proj, both out-proj, MoE down) peel the first K-iteration with SrcC=0 instead of zeroing 128 accumulators per unit
# speedup vs baseline: 1.0084x; 1.0084x over previous
.LBB0_301:
	s_add_u32 s0, s2, 0x100
	s_addc_u32 s1, s3, 0
	s_add_u32 s52, s18, 0x100
	s_addc_u32 s53, s19, 0
	s_add_u32 s2, s2, 0x80
	s_addc_u32 s3, s3, 0
	s_mov_b32 s87, -2
	s_waitcnt vmcnt(0)
	s_cmp_eq_u32 s87, 12
	s_cselect_b32 s14, s48, s0
	s_cselect_b32 s15, s49, s1
	s_cselect_b32 s18, s50, s52
	s_cselect_b32 s19, s51, s53
	s_add_u32 s28, s14, 0x80
	s_addc_u32 s29, s15, 0
	s_add_i32 s90, 0, 0x10000
	v_add_u32_e32 v144, s90, v35
	ds_read_b128 v[132:135], v144
	ds_read_b128 v[136:139], v144 offset:1024
	ds_read_b128 v[140:143], v144 offset:2048
	ds_read_b128 v[144:147], v144 offset:3072
	s_mov_b64 s[88:89], s[2:3]
	ds_read_b128 v[160:163], v172
	ds_read_b128 v[164:167], v172 offset:1024
	ds_read_b128 v[174:177], v172 offset:2048
	ds_read_b128 v[178:181], v172 offset:3072
	ds_read_b128 v[182:185], v172 offset:4096
	ds_read_b128 v[186:189], v172 offset:5120
	ds_read_b128 v[190:193], v172 offset:6144
	ds_read_b128 v[194:197], v172 offset:7168
	s_add_i32 m0, s71, 0xc000
	v_lshl_add_u64 v[168:169], s[88:89], 0, v[156:157]
	global_load_lds_dwordx4 v[168:169], off
	v_lshl_add_u64 v[168:169], s[88:89], 0, v[158:159]
	s_add_i32 m0, s71, 0xe000
	s_nop 0
	global_load_lds_dwordx4 v[168:169], off
	s_waitcnt lgkmcnt(8)
	s_barrier
	s_waitcnt lgkmcnt(0)
	s_setprio 1
	s_waitcnt lgkmcnt(0)
	v_mfma_f32_16x16x32_bf16 v[128:131], v[132:135], v[160:163], 0
	v_mfma_f32_16x16x32_bf16 v[124:127], v[140:143], v[160:163], 0
	v_mfma_f32_16x16x32_bf16 v[120:123], v[132:135], v[174:177], 0
	v_mfma_f32_16x16x32_bf16 v[116:119], v[140:143], v[174:177], 0
	v_mfma_f32_16x16x32_bf16 v[104:107], v[132:135], v[182:185], 0
	v_mfma_f32_16x16x32_bf16 v[100:103], v[140:143], v[182:185], 0
	v_mfma_f32_16x16x32_bf16 v[88:91], v[132:135], v[190:193], 0
	v_mfma_f32_16x16x32_bf16 v[84:87], v[140:143], v[190:193], 0
	v_mfma_f32_16x16x32_bf16 v[128:131], v[136:139], v[164:167], v[128:131]
	v_mfma_f32_16x16x32_bf16 v[124:127], v[144:147], v[164:167], v[124:127]
	v_mfma_f32_16x16x32_bf16 v[120:123], v[136:139], v[178:181], v[120:123]
	v_mfma_f32_16x16x32_bf16 v[116:119], v[144:147], v[178:181], v[116:119]
	v_mfma_f32_16x16x32_bf16 v[104:107], v[136:139], v[186:189], v[104:107]
	v_mfma_f32_16x16x32_bf16 v[100:103], v[144:147], v[186:189], v[100:103]
	v_mfma_f32_16x16x32_bf16 v[88:91], v[136:139], v[194:197], v[88:91]
	v_mfma_f32_16x16x32_bf16 v[84:87], v[144:147], v[194:197], v[84:87]
	s_setprio 0
	s_barrier
	s_add_i32 s91, 0, 0x14000
	v_add_u32_e32 v168, s91, v35
	s_mov_b64 s[88:89], s[18:19]
	s_add_i32 s90, s90, s58
	ds_read_b128 v[198:201], v168
	ds_read_b128 v[202:205], v168 offset:1024
	ds_read_b128 v[206:209], v168 offset:2048
	ds_read_b128 v[218:221], v168 offset:3072
	s_mov_b32 m0, s90
	v_lshl_add_u64 v[168:169], s[88:89], 0, v[150:151]
	global_load_lds_dwordx4 v[168:169], off
	v_lshl_add_u64 v[168:169], s[88:89], 0, v[148:149]
	s_add_i32 m0, s90, 0x2000
	s_nop 0
	global_load_lds_dwordx4 v[168:169], off
	s_barrier
	s_waitcnt lgkmcnt(0)
	s_setprio 1
	s_waitcnt lgkmcnt(0)
	v_mfma_f32_16x16x32_bf16 v[112:115], v[198:201], v[160:163], 0
	v_mfma_f32_16x16x32_bf16 v[108:111], v[206:209], v[160:163], 0
	v_mfma_f32_16x16x32_bf16 v[96:99], v[198:201], v[174:177], 0
	v_mfma_f32_16x16x32_bf16 v[92:95], v[206:209], v[174:177], 0
	v_mfma_f32_16x16x32_bf16 v[80:83], v[198:201], v[182:185], 0
	v_mfma_f32_16x16x32_bf16 v[76:79], v[206:209], v[182:185], 0
	v_mfma_f32_16x16x32_bf16 v[72:75], v[198:201], v[190:193], 0
	v_mfma_f32_16x16x32_bf16 v[68:71], v[206:209], v[190:193], 0
	v_mfma_f32_16x16x32_bf16 v[112:115], v[202:205], v[164:167], v[112:115]
	v_mfma_f32_16x16x32_bf16 v[108:111], v[218:221], v[164:167], v[108:111]
	v_mfma_f32_16x16x32_bf16 v[96:99], v[202:205], v[178:181], v[96:99]
	v_mfma_f32_16x16x32_bf16 v[92:95], v[218:221], v[178:181], v[92:95]
	v_mfma_f32_16x16x32_bf16 v[80:83], v[202:205], v[186:189], v[80:83]
	v_mfma_f32_16x16x32_bf16 v[76:79], v[218:221], v[186:189], v[76:79]
	v_mfma_f32_16x16x32_bf16 v[72:75], v[202:205], v[194:197], v[72:75]
	v_mfma_f32_16x16x32_bf16 v[68:71], v[218:221], v[194:197], v[68:71]
	s_setprio 0
	s_mov_b64 s[88:89], s[14:15]
	s_mov_b32 m0, s71
	s_barrier
	ds_read_b128 v[160:163], v172 offset:16384
	ds_read_b128 v[164:167], v172 offset:17408
	ds_read_b128 v[174:177], v172 offset:18432
	ds_read_b128 v[178:181], v172 offset:19456
	ds_read_b128 v[182:185], v172 offset:20480
	ds_read_b128 v[186:189], v172 offset:21504
	ds_read_b128 v[190:193], v172 offset:22528
	ds_read_b128 v[194:197], v172 offset:23552
	s_nop 0
	v_lshl_add_u64 v[168:169], s[88:89], 0, v[152:153]
	global_load_lds_dwordx4 v[168:169], off
	v_lshl_add_u64 v[168:169], s[88:89], 0, v[154:155]
	s_mov_b32 m0, s37
	s_nop 0
	global_load_lds_dwordx4 v[168:169], off
	s_barrier
	s_waitcnt lgkmcnt(0)
	s_setprio 1
	s_waitcnt lgkmcnt(0)
	v_mfma_f32_16x16x32_bf16 v[64:67], v[132:135], v[160:163], 0
	v_mfma_f32_16x16x32_bf16 v[60:63], v[140:143], v[160:163], 0
	v_mfma_f32_16x16x32_bf16 v[56:59], v[132:135], v[174:177], 0
	v_mfma_f32_16x16x32_bf16 v[52:55], v[140:143], v[174:177], 0
	v_mfma_f32_16x16x32_bf16 v[40:43], v[132:135], v[182:185], 0
	v_mfma_f32_16x16x32_bf16 v[36:39], v[140:143], v[182:185], 0
	v_mfma_f32_16x16x32_bf16 v[22:25], v[132:135], v[190:193], 0
	v_mfma_f32_16x16x32_bf16 v[18:21], v[140:143], v[190:193], 0
	v_mfma_f32_16x16x32_bf16 v[64:67], v[136:139], v[164:167], v[64:67]
	v_mfma_f32_16x16x32_bf16 v[60:63], v[144:147], v[164:167], v[60:63]
	v_mfma_f32_16x16x32_bf16 v[56:59], v[136:139], v[178:181], v[56:59]
	v_mfma_f32_16x16x32_bf16 v[52:55], v[144:147], v[178:181], v[52:55]
	v_mfma_f32_16x16x32_bf16 v[40:43], v[136:139], v[186:189], v[40:43]
	v_mfma_f32_16x16x32_bf16 v[36:39], v[144:147], v[186:189], v[36:39]
	v_mfma_f32_16x16x32_bf16 v[22:25], v[136:139], v[194:197], v[22:25]
	v_mfma_f32_16x16x32_bf16 v[18:21], v[144:147], v[194:197], v[18:21]
	s_setprio 0
	s_barrier
	s_add_u32 s88, s18, 0x40000
	s_addc_u32 s89, s19, 0
	s_add_i32 s90, s91, s58
	s_mov_b32 m0, s90
	v_lshl_add_u64 v[132:133], s[88:89], 0, v[150:151]
	global_load_lds_dwordx4 v[132:133], off
	v_lshl_add_u64 v[132:133], s[88:89], 0, v[148:149]
	s_add_i32 m0, s90, 0x2000
	s_nop 0
	global_load_lds_dwordx4 v[132:133], off
	s_waitcnt vmcnt(6)
	s_barrier
	s_setprio 1
	v_mfma_f32_16x16x32_bf16 v[48:51], v[198:201], v[160:163], 0
	v_mfma_f32_16x16x32_bf16 v[44:47], v[206:209], v[160:163], 0
	v_mfma_f32_16x16x32_bf16 v[30:33], v[198:201], v[174:177], 0
	v_mfma_f32_16x16x32_bf16 v[26:29], v[206:209], v[174:177], 0
	v_mfma_f32_16x16x32_bf16 v[14:17], v[198:201], v[182:185], 0
	v_mfma_f32_16x16x32_bf16 v[10:13], v[206:209], v[182:185], 0
	v_mfma_f32_16x16x32_bf16 v[6:9], v[198:201], v[190:193], 0
	v_mfma_f32_16x16x32_bf16 v[2:5], v[206:209], v[190:193], 0
	v_mfma_f32_16x16x32_bf16 v[48:51], v[202:205], v[164:167], v[48:51]
	v_mfma_f32_16x16x32_bf16 v[44:47], v[218:221], v[164:167], v[44:47]
	v_mfma_f32_16x16x32_bf16 v[30:33], v[202:205], v[178:181], v[30:33]
	v_mfma_f32_16x16x32_bf16 v[26:29], v[218:221], v[178:181], v[26:29]
	v_mfma_f32_16x16x32_bf16 v[14:17], v[202:205], v[186:189], v[14:17]
	v_mfma_f32_16x16x32_bf16 v[10:13], v[218:221], v[186:189], v[10:13]
	v_mfma_f32_16x16x32_bf16 v[6:9], v[202:205], v[194:197], v[6:9]
	v_mfma_f32_16x16x32_bf16 v[2:5], v[218:221], v[194:197], v[2:5]
	s_setprio 0
	s_add_i32 s88, 0, 0x18000
	v_add_u32_e32 v144, s88, v35
	s_barrier
	ds_read_b128 v[132:135], v144
	ds_read_b128 v[136:139], v144 offset:1024
	ds_read_b128 v[140:143], v144 offset:2048
	ds_read_b128 v[144:147], v144 offset:3072
	s_mov_b32 m0, s76
	ds_read_b128 v[160:163], v172 offset:32768
	ds_read_b128 v[164:167], v172 offset:33792
	ds_read_b128 v[174:177], v172 offset:34816
	ds_read_b128 v[178:181], v172 offset:35840
	ds_read_b128 v[182:185], v172 offset:36864
	ds_read_b128 v[186:189], v172 offset:37888
	ds_read_b128 v[190:193], v172 offset:38912
	ds_read_b128 v[194:197], v172 offset:39936
	s_nop 0
	v_lshl_add_u64 v[168:169], s[14:15], 0, v[156:157]
	global_load_lds_dwordx4 v[168:169], off
	v_lshl_add_u64 v[168:169], s[14:15], 0, v[158:159]
	s_mov_b32 m0, s77
	s_nop 0
	global_load_lds_dwordx4 v[168:169], off
	s_waitcnt lgkmcnt(8)
	s_barrier
	s_waitcnt lgkmcnt(0)
	s_setprio 1
	s_waitcnt lgkmcnt(0)
	v_mfma_f32_16x16x32_bf16 v[128:131], v[132:135], v[160:163], v[128:131]
	v_mfma_f32_16x16x32_bf16 v[124:127], v[140:143], v[160:163], v[124:127]
	v_mfma_f32_16x16x32_bf16 v[120:123], v[132:135], v[174:177], v[120:123]
	v_mfma_f32_16x16x32_bf16 v[116:119], v[140:143], v[174:177], v[116:119]
	v_mfma_f32_16x16x32_bf16 v[104:107], v[132:135], v[182:185], v[104:107]
	v_mfma_f32_16x16x32_bf16 v[100:103], v[140:143], v[182:185], v[100:103]
	v_mfma_f32_16x16x32_bf16 v[88:91], v[132:135], v[190:193], v[88:91]
	v_mfma_f32_16x16x32_bf16 v[84:87], v[140:143], v[190:193], v[84:87]
	v_mfma_f32_16x16x32_bf16 v[128:131], v[136:139], v[164:167], v[128:131]
	v_mfma_f32_16x16x32_bf16 v[124:127], v[144:147], v[164:167], v[124:127]
	v_mfma_f32_16x16x32_bf16 v[120:123], v[136:139], v[178:181], v[120:123]
	v_mfma_f32_16x16x32_bf16 v[116:119], v[144:147], v[178:181], v[116:119]
	v_mfma_f32_16x16x32_bf16 v[104:107], v[136:139], v[186:189], v[104:107]
	v_mfma_f32_16x16x32_bf16 v[100:103], v[144:147], v[186:189], v[100:103]
	v_mfma_f32_16x16x32_bf16 v[88:91], v[136:139], v[194:197], v[88:91]
	v_mfma_f32_16x16x32_bf16 v[84:87], v[144:147], v[194:197], v[84:87]
	s_setprio 0
	s_barrier
	s_add_i32 s89, 0, 0x1c000
	s_add_u32 s14, s18, 0x80
	v_add_u32_e32 v168, s89, v35
	s_addc_u32 s15, s19, 0
	s_add_i32 s88, s88, s58
	ds_read_b128 v[198:201], v168
	ds_read_b128 v[202:205], v168 offset:1024
	ds_read_b128 v[206:209], v168 offset:2048
	ds_read_b128 v[218:221], v168 offset:3072
	s_mov_b32 m0, s88
	v_lshl_add_u64 v[168:169], s[14:15], 0, v[150:151]
	global_load_lds_dwordx4 v[168:169], off
	v_lshl_add_u64 v[168:169], s[14:15], 0, v[148:149]
	s_add_i32 m0, s88, 0x2000
	s_nop 0
	global_load_lds_dwordx4 v[168:169], off
	s_barrier
	s_waitcnt lgkmcnt(0)
	s_setprio 1
	s_waitcnt lgkmcnt(0)
	v_mfma_f32_16x16x32_bf16 v[112:115], v[198:201], v[160:163], v[112:115]
	v_mfma_f32_16x16x32_bf16 v[108:111], v[206:209], v[160:163], v[108:111]
	v_mfma_f32_16x16x32_bf16 v[96:99], v[198:201], v[174:177], v[96:99]
	v_mfma_f32_16x16x32_bf16 v[92:95], v[206:209], v[174:177], v[92:95]
	v_mfma_f32_16x16x32_bf16 v[80:83], v[198:201], v[182:185], v[80:83]
	v_mfma_f32_16x16x32_bf16 v[76:79], v[206:209], v[182:185], v[76:79]
	v_mfma_f32_16x16x32_bf16 v[72:75], v[198:201], v[190:193], v[72:75]
	v_mfma_f32_16x16x32_bf16 v[68:71], v[206:209], v[190:193], v[68:71]
	v_mfma_f32_16x16x32_bf16 v[112:115], v[202:205], v[164:167], v[112:115]
	v_mfma_f32_16x16x32_bf16 v[108:111], v[218:221], v[164:167], v[108:111]
	v_mfma_f32_16x16x32_bf16 v[96:99], v[202:205], v[178:181], v[96:99]
	v_mfma_f32_16x16x32_bf16 v[92:95], v[218:221], v[178:181], v[92:95]
	v_mfma_f32_16x16x32_bf16 v[80:83], v[202:205], v[186:189], v[80:83]
	v_mfma_f32_16x16x32_bf16 v[76:79], v[218:221], v[186:189], v[76:79]
	v_mfma_f32_16x16x32_bf16 v[72:75], v[202:205], v[194:197], v[72:75]
	v_mfma_f32_16x16x32_bf16 v[68:71], v[218:221], v[194:197], v[68:71]
	s_setprio 0
	s_mov_b32 m0, s80
	s_barrier
	ds_read_b128 v[160:163], v172 offset:49152
	ds_read_b128 v[164:167], v172 offset:50176
	ds_read_b128 v[174:177], v172 offset:51200
	ds_read_b128 v[178:181], v172 offset:52224
	ds_read_b128 v[182:185], v172 offset:53248
	ds_read_b128 v[186:189], v172 offset:54272
	ds_read_b128 v[190:193], v172 offset:55296
	ds_read_b128 v[194:197], v172 offset:56320
	s_nop 0
	v_lshl_add_u64 v[168:169], s[28:29], 0, v[152:153]
	global_load_lds_dwordx4 v[168:169], off
	v_lshl_add_u64 v[168:169], s[28:29], 0, v[154:155]
	s_mov_b32 m0, s81
	s_nop 0
	global_load_lds_dwordx4 v[168:169], off
	s_barrier
	s_waitcnt lgkmcnt(0)
	s_setprio 1
	s_waitcnt lgkmcnt(0)
	v_mfma_f32_16x16x32_bf16 v[64:67], v[132:135], v[160:163], v[64:67]
	v_mfma_f32_16x16x32_bf16 v[60:63], v[140:143], v[160:163], v[60:63]
	v_mfma_f32_16x16x32_bf16 v[56:59], v[132:135], v[174:177], v[56:59]
	v_mfma_f32_16x16x32_bf16 v[52:55], v[140:143], v[174:177], v[52:55]
	v_mfma_f32_16x16x32_bf16 v[40:43], v[132:135], v[182:185], v[40:43]
	v_mfma_f32_16x16x32_bf16 v[36:39], v[140:143], v[182:185], v[36:39]
	v_mfma_f32_16x16x32_bf16 v[22:25], v[132:135], v[190:193], v[22:25]
	v_mfma_f32_16x16x32_bf16 v[18:21], v[140:143], v[190:193], v[18:21]
	v_mfma_f32_16x16x32_bf16 v[64:67], v[136:139], v[164:167], v[64:67]
	v_mfma_f32_16x16x32_bf16 v[60:63], v[144:147], v[164:167], v[60:63]
	v_mfma_f32_16x16x32_bf16 v[56:59], v[136:139], v[178:181], v[56:59]
	v_mfma_f32_16x16x32_bf16 v[52:55], v[144:147], v[178:181], v[52:55]
	v_mfma_f32_16x16x32_bf16 v[40:43], v[136:139], v[186:189], v[40:43]
	v_mfma_f32_16x16x32_bf16 v[36:39], v[144:147], v[186:189], v[36:39]
	v_mfma_f32_16x16x32_bf16 v[22:25], v[136:139], v[194:197], v[22:25]
	v_mfma_f32_16x16x32_bf16 v[18:21], v[144:147], v[194:197], v[18:21]
	s_setprio 0
	s_barrier
	s_add_u32 s14, s18, 0x40080
	s_addc_u32 s15, s19, 0
	s_add_i32 s18, s89, s58
	s_mov_b32 m0, s18
	v_lshl_add_u64 v[132:133], s[14:15], 0, v[150:151]
	global_load_lds_dwordx4 v[132:133], off
	v_lshl_add_u64 v[132:133], s[14:15], 0, v[148:149]
	s_add_i32 m0, s18, 0x2000
	s_nop 0
	global_load_lds_dwordx4 v[132:133], off
	s_waitcnt vmcnt(6)
	s_barrier
	s_setprio 1
	v_mfma_f32_16x16x32_bf16 v[48:51], v[198:201], v[160:163], v[48:51]
	v_mfma_f32_16x16x32_bf16 v[44:47], v[206:209], v[160:163], v[44:47]
	v_mfma_f32_16x16x32_bf16 v[30:33], v[198:201], v[174:177], v[30:33]
	v_mfma_f32_16x16x32_bf16 v[26:29], v[206:209], v[174:177], v[26:29]
	v_mfma_f32_16x16x32_bf16 v[14:17], v[198:201], v[182:185], v[14:17]
	v_mfma_f32_16x16x32_bf16 v[10:13], v[206:209], v[182:185], v[10:13]
	v_mfma_f32_16x16x32_bf16 v[6:9], v[198:201], v[190:193], v[6:9]
	v_mfma_f32_16x16x32_bf16 v[2:5], v[206:209], v[190:193], v[2:5]
	v_mfma_f32_16x16x32_bf16 v[48:51], v[202:205], v[164:167], v[48:51]
	v_mfma_f32_16x16x32_bf16 v[44:47], v[218:221], v[164:167], v[44:47]
	v_mfma_f32_16x16x32_bf16 v[30:33], v[202:205], v[178:181], v[30:33]
	v_mfma_f32_16x16x32_bf16 v[26:29], v[218:221], v[178:181], v[26:29]
	v_mfma_f32_16x16x32_bf16 v[14:17], v[202:205], v[186:189], v[14:17]
	v_mfma_f32_16x16x32_bf16 v[10:13], v[218:221], v[186:189], v[10:13]
	v_mfma_f32_16x16x32_bf16 v[6:9], v[202:205], v[194:197], v[6:9]
	v_mfma_f32_16x16x32_bf16 v[2:5], v[218:221], v[194:197], v[2:5]
	s_setprio 0
	s_add_i32 s87, s87, 2
	s_add_u32 s0, s0, 0x100
	s_addc_u32 s1, s1, 0
	s_add_u32 s52, s52, 0x100
	s_addc_u32 s53, s53, 0
	s_add_u32 s2, s2, 0x100
	s_addc_u32 s3, s3, 0
	s_cmp_gt_u32 s87, 13
	s_barrier
	s_cbranch_scc0 .LBB0_302
	s_branch .Lpeel_exit_0

.Lpeel_exit_0:
	s_lshl_b32 s14, s41, 8
	s_mov_b32 s0, 0
	s_add_i32 s14, s14, s13
	v_add_u32_e32 v132, s0, v1
	s_lshl_b32 s28, s40, 8
	v_add_u32_e32 v160, s14, v132
	s_cmp_lt_i32 s28, s79
	s_mov_b64 s[0:1], -1
	s_cbranch_scc1 .LBB0_305
	s_sub_i32 s0, s40, s82
	v_lshl_add_u32 v138, s0, 7, v171
	v_pk_mul_f32 v[136:137], v[130:131], v[114:115]
	v_pk_mul_f32 v[134:135], v[128:129], v[112:113]
	v_pk_mul_f32 v[140:141], v[126:127], v[110:111]
	v_ashrrev_i32_e32 v139, 31, v138
	v_cvt_pk_bf16_f32 v134, v134, v135
	v_cvt_pk_bf16_f32 v135, v136, v137
	v_cvt_pk_bf16_f32 v137, v140, v141
	v_mad_i64_i32 v[140:141], s[0:1], v160, s78, 0
	v_pk_mul_f32 v[142:143], v[124:125], v[108:109]
	v_lshl_add_u64 v[140:141], v[140:141], 1, s[16:17]
	v_lshlrev_b64 v[138:139], 1, v[138:139]
	v_cvt_pk_bf16_f32 v136, v142, v143
	v_lshl_add_u64 v[140:141], v[140:141], 0, v[138:139]
	global_store_dwordx4 v[140:141], v[134:137], off
	v_pk_mul_f32 v[140:141], v[118:119], v[94:95]
	v_add_u32_e32 v133, 16, v160
	v_pk_mul_f32 v[136:137], v[122:123], v[98:99]
	v_pk_mul_f32 v[134:135], v[120:121], v[96:97]
	v_pk_mul_f32 v[142:143], v[116:117], v[92:93]
	v_cvt_pk_bf16_f32 v134, v134, v135
	v_cvt_pk_bf16_f32 v135, v136, v137
	v_cvt_pk_bf16_f32 v137, v140, v141
	v_mad_i64_i32 v[140:141], s[0:1], v133, s78, 0
	v_lshl_add_u64 v[140:141], v[140:141], 1, s[16:17]
	v_cvt_pk_bf16_f32 v136, v142, v143
	v_lshl_add_u64 v[140:141], v[140:141], 0, v[138:139]
	global_store_dwordx4 v[140:141], v[134:137], off
	v_pk_mul_f32 v[140:141], v[102:103], v[78:79]
	v_add_u32_e32 v133, 32, v160
	v_pk_mul_f32 v[136:137], v[106:107], v[82:83]
	v_pk_mul_f32 v[134:135], v[104:105], v[80:81]
	v_pk_mul_f32 v[142:143], v[100:101], v[76:77]
	v_cvt_pk_bf16_f32 v134, v134, v135
	v_cvt_pk_bf16_f32 v135, v136, v137
	v_cvt_pk_bf16_f32 v137, v140, v141
	v_mad_i64_i32 v[140:141], s[0:1], v133, s78, 0
	v_lshl_add_u64 v[140:141], v[140:141], 1, s[16:17]
	v_cvt_pk_bf16_f32 v136, v142, v143
	v_lshl_add_u64 v[140:141], v[140:141], 0, v[138:139]
	global_store_dwordx4 v[140:141], v[134:137], off
	v_pk_mul_f32 v[140:141], v[86:87], v[70:71]
	v_add_u32_e32 v133, 48, v160
	v_pk_mul_f32 v[136:137], v[90:91], v[74:75]
	v_pk_mul_f32 v[134:135], v[88:89], v[72:73]
	v_pk_mul_f32 v[142:143], v[84:85], v[68:69]
	v_cvt_pk_bf16_f32 v134, v134, v135
	v_cvt_pk_bf16_f32 v135, v136, v137
	v_cvt_pk_bf16_f32 v137, v140, v141
	v_mad_i64_i32 v[140:141], s[0:1], v133, s78, 0
	v_lshl_add_u64 v[140:141], v[140:141], 1, s[16:17]
	v_cvt_pk_bf16_f32 v136, v142, v143
	v_lshl_add_u64 v[140:141], v[140:141], 0, v[138:139]
	global_store_dwordx4 v[140:141], v[134:137], off
	v_add_u32_e32 v133, 0x80, v160
	v_pk_mul_f32 v[140:141], v[62:63], v[46:47]
	v_pk_mul_f32 v[136:137], v[66:67], v[50:51]
	v_pk_mul_f32 v[134:135], v[64:65], v[48:49]
	v_pk_mul_f32 v[142:143], v[60:61], v[44:45]
	v_cvt_pk_bf16_f32 v134, v134, v135
	v_cvt_pk_bf16_f32 v135, v136, v137
	v_cvt_pk_bf16_f32 v137, v140, v141
	v_mad_i64_i32 v[140:141], s[0:1], v133, s78, 0
	v_lshl_add_u64 v[140:141], v[140:141], 1, s[16:17]
	v_cvt_pk_bf16_f32 v136, v142, v143
	v_lshl_add_u64 v[140:141], v[140:141], 0, v[138:139]
	global_store_dwordx4 v[140:141], v[134:137], off
	v_pk_mul_f32 v[140:141], v[54:55], v[28:29]
	v_add_u32_e32 v133, 0x90, v160
	v_pk_mul_f32 v[136:137], v[58:59], v[32:33]
	v_pk_mul_f32 v[134:135], v[56:57], v[30:31]
	v_pk_mul_f32 v[142:143], v[52:53], v[26:27]
	v_cvt_pk_bf16_f32 v134, v134, v135
	v_cvt_pk_bf16_f32 v135, v136, v137
	v_cvt_pk_bf16_f32 v137, v140, v141
	v_mad_i64_i32 v[140:141], s[0:1], v133, s78, 0
	v_lshl_add_u64 v[140:141], v[140:141], 1, s[16:17]
	v_cvt_pk_bf16_f32 v136, v142, v143
	v_lshl_add_u64 v[140:141], v[140:141], 0, v[138:139]
	global_store_dwordx4 v[140:141], v[134:137], off
	v_pk_mul_f32 v[140:141], v[38:39], v[12:13]
	v_add_u32_e32 v133, 0xa0, v160
	v_pk_mul_f32 v[136:137], v[42:43], v[16:17]
	v_pk_mul_f32 v[134:135], v[40:41], v[14:15]
	v_pk_mul_f32 v[142:143], v[36:37], v[10:11]
	v_cvt_pk_bf16_f32 v134, v134, v135
	v_cvt_pk_bf16_f32 v135, v136, v137
	v_cvt_pk_bf16_f32 v137, v140, v141
	v_mad_i64_i32 v[140:141], s[0:1], v133, s78, 0
	v_lshl_add_u64 v[140:141], v[140:141], 1, s[16:17]
	v_cvt_pk_bf16_f32 v136, v142, v143
	v_lshl_add_u64 v[140:141], v[140:141], 0, v[138:139]
	global_store_dwordx4 v[140:141], v[134:137], off
	v_pk_mul_f32 v[140:141], v[20:21], v[4:5]
	v_add_u32_e32 v133, 0xb0, v160
	v_pk_mul_f32 v[136:137], v[24:25], v[8:9]
	v_pk_mul_f32 v[134:135], v[22:23], v[6:7]
	v_pk_mul_f32 v[142:143], v[18:19], v[2:3]
	v_cvt_pk_bf16_f32 v134, v134, v135
	v_cvt_pk_bf16_f32 v135, v136, v137
	v_cvt_pk_bf16_f32 v137, v140, v141
	v_mad_i64_i32 v[140:141], s[0:1], v133, s78, 0
	v_lshl_add_u64 v[140:141], v[140:141], 1, s[16:17]
	v_cvt_pk_bf16_f32 v136, v142, v143
	v_lshl_add_u64 v[138:139], v[140:141], 0, v[138:139]
	s_mov_b64 s[0:1], 0
	global_store_dwordx4 v[138:139], v[134:137], off

.LBB0_995:
	s_add_u32 s0, s36, 0x100
	s_addc_u32 s1, s37, 0
	s_add_u32 s79, s40, 0x100
	s_addc_u32 s80, s41, 0
	s_add_u32 s36, s36, 0x80
	s_addc_u32 s37, s37, 0
	s_mov_b32 s81, -2
	s_cmp_eq_u32 s81, 4
	s_cselect_b32 s44, s2, s0
	s_cselect_b32 s45, s3, s1
	s_cselect_b32 s40, s18, s79
	s_cselect_b32 s41, s19, s80
	s_waitcnt lgkmcnt(0)
	s_add_u32 s42, s44, 0x80
	s_addc_u32 s43, s45, 0
	s_add_i32 s86, 0, 0x10000
	v_add_u32_e32 v6, s86, v179
	ds_read_b128 v[10:13], v6
	ds_read_b128 v[14:17], v6 offset:1024
	ds_read_b128 v[2:5], v6 offset:2048
	ds_read_b128 v[6:9], v6 offset:3072
	s_mov_b64 s[82:83], s[36:37]
	ds_read_b128 v[182:185], v181
	ds_read_b128 v[186:189], v181 offset:1024
	ds_read_b128 v[190:193], v181 offset:2048
	ds_read_b128 v[194:197], v181 offset:3072
	ds_read_b128 v[198:201], v181 offset:4096
	ds_read_b128 v[202:205], v181 offset:5120
	ds_read_b128 v[218:221], v181 offset:6144
	ds_read_b128 v[222:225], v181 offset:7168
	s_add_i32 m0, s49, 0xc000
	v_lshl_add_u64 v[18:19], s[82:83], 0, v[172:173]
	global_load_lds_dwordx4 v[18:19], off
	v_lshl_add_u64 v[18:19], s[82:83], 0, v[174:175]
	s_add_i32 m0, s49, 0xe000
	s_nop 0
	global_load_lds_dwordx4 v[18:19], off
	s_waitcnt lgkmcnt(8)
	s_barrier
	s_waitcnt lgkmcnt(0)
	s_setprio 1
	s_waitcnt lgkmcnt(0)
	v_mfma_scale_f32_16x16x128_f8f6f4 v[160:163], v[10:17], v[182:189], 0, v176, v35 op_sel_hi:[0,0,0]
	v_mfma_scale_f32_16x16x128_f8f6f4 v[156:159], v[2:9], v[182:189], 0, v176, v35 op_sel_hi:[0,0,0]
	v_mfma_scale_f32_16x16x128_f8f6f4 v[148:151], v[10:17], v[190:197], 0, v176, v35 op_sel_hi:[0,0,0]
	v_mfma_scale_f32_16x16x128_f8f6f4 v[140:143], v[2:9], v[190:197], 0, v176, v35 op_sel_hi:[0,0,0]
	v_mfma_scale_f32_16x16x128_f8f6f4 v[132:135], v[10:17], v[198:205], 0, v176, v35 op_sel_hi:[0,0,0]
	v_mfma_scale_f32_16x16x128_f8f6f4 v[124:127], v[2:9], v[198:205], 0, v176, v35 op_sel_hi:[0,0,0]
	v_mfma_scale_f32_16x16x128_f8f6f4 v[116:119], v[10:17], v[218:225], 0, v176, v35 op_sel_hi:[0,0,0]
	v_mfma_scale_f32_16x16x128_f8f6f4 v[108:111], v[2:9], v[218:225], 0, v176, v35 op_sel_hi:[0,0,0]
	s_setprio 0
	s_barrier
	s_add_i32 s82, 0, 0x14000
	v_add_u32_e32 v22, s82, v179
	s_mov_b64 s[84:85], s[40:41]
	s_add_i32 s83, s86, s17
	ds_read_b128 v[26:29], v22
	ds_read_b128 v[30:33], v22 offset:1024
	ds_read_b128 v[18:21], v22 offset:2048
	ds_read_b128 v[22:25], v22 offset:3072
	s_mov_b32 m0, s83
	v_lshl_add_u64 v[206:207], s[84:85], 0, v[166:167]
	global_load_lds_dwordx4 v[206:207], off
	v_lshl_add_u64 v[206:207], s[84:85], 0, v[164:165]
	s_add_i32 m0, s83, 0x2000
	s_nop 0
	global_load_lds_dwordx4 v[206:207], off
	s_barrier
	s_waitcnt lgkmcnt(0)
	s_setprio 1
	s_waitcnt lgkmcnt(0)
	v_mfma_scale_f32_16x16x128_f8f6f4 v[152:155], v[26:33], v[182:189], 0, v177, v35 op_sel_hi:[0,0,0]
	v_mfma_scale_f32_16x16x128_f8f6f4 v[144:147], v[18:25], v[182:189], 0, v177, v35 op_sel_hi:[0,0,0]
	v_mfma_scale_f32_16x16x128_f8f6f4 v[136:139], v[26:33], v[190:197], 0, v177, v35 op_sel_hi:[0,0,0]
	v_mfma_scale_f32_16x16x128_f8f6f4 v[128:131], v[18:25], v[190:197], 0, v177, v35 op_sel_hi:[0,0,0]
	v_mfma_scale_f32_16x16x128_f8f6f4 v[120:123], v[26:33], v[198:205], 0, v177, v35 op_sel_hi:[0,0,0]
	v_mfma_scale_f32_16x16x128_f8f6f4 v[112:115], v[18:25], v[198:205], 0, v177, v35 op_sel_hi:[0,0,0]
	v_mfma_scale_f32_16x16x128_f8f6f4 v[104:107], v[26:33], v[218:225], 0, v177, v35 op_sel_hi:[0,0,0]
	v_mfma_scale_f32_16x16x128_f8f6f4 v[100:103], v[18:25], v[218:225], 0, v177, v35 op_sel_hi:[0,0,0]
	s_setprio 0
	s_mov_b64 s[84:85], s[44:45]
	s_mov_b32 m0, s49
	s_barrier
	ds_read_b128 v[182:185], v181 offset:16384
	ds_read_b128 v[186:189], v181 offset:17408
	ds_read_b128 v[190:193], v181 offset:18432
	ds_read_b128 v[194:197], v181 offset:19456
	ds_read_b128 v[198:201], v181 offset:20480
	ds_read_b128 v[202:205], v181 offset:21504
	ds_read_b128 v[218:221], v181 offset:22528
	ds_read_b128 v[222:225], v181 offset:23552
	s_nop 0
	v_lshl_add_u64 v[206:207], s[84:85], 0, v[168:169]
	global_load_lds_dwordx4 v[206:207], off
	v_lshl_add_u64 v[206:207], s[84:85], 0, v[170:171]
	s_mov_b32 m0, s56
	s_nop 0
	global_load_lds_dwordx4 v[206:207], off
	s_barrier
	s_waitcnt lgkmcnt(0)
	s_setprio 1
	s_waitcnt lgkmcnt(0)
	v_mfma_scale_f32_16x16x128_f8f6f4 v[96:99], v[10:17], v[182:189], 0, v176, v35 op_sel_hi:[0,0,0]
	v_mfma_scale_f32_16x16x128_f8f6f4 v[92:95], v[2:9], v[182:189], 0, v176, v35 op_sel_hi:[0,0,0]
	v_mfma_scale_f32_16x16x128_f8f6f4 v[84:87], v[10:17], v[190:197], 0, v176, v35 op_sel_hi:[0,0,0]
	v_mfma_scale_f32_16x16x128_f8f6f4 v[76:79], v[2:9], v[190:197], 0, v176, v35 op_sel_hi:[0,0,0]
	v_mfma_scale_f32_16x16x128_f8f6f4 v[68:71], v[10:17], v[198:205], 0, v176, v35 op_sel_hi:[0,0,0]
	v_mfma_scale_f32_16x16x128_f8f6f4 v[60:63], v[2:9], v[198:205], 0, v176, v35 op_sel_hi:[0,0,0]
	v_mfma_scale_f32_16x16x128_f8f6f4 v[52:55], v[10:17], v[218:225], 0, v176, v35 op_sel_hi:[0,0,0]
	v_mfma_scale_f32_16x16x128_f8f6f4 v[44:47], v[2:9], v[218:225], 0, v176, v35 op_sel_hi:[0,0,0]
	s_setprio 0
	s_barrier
	s_add_u32 s84, s40, 0x20000
	s_addc_u32 s85, s41, 0
	s_add_i32 s82, s82, s17
	s_mov_b32 m0, s82
	v_lshl_add_u64 v[2:3], s[84:85], 0, v[166:167]
	global_load_lds_dwordx4 v[2:3], off
	v_lshl_add_u64 v[2:3], s[84:85], 0, v[164:165]
	s_add_i32 m0, s82, 0x2000
	s_nop 0
	global_load_lds_dwordx4 v[2:3], off
	s_waitcnt vmcnt(6)
	s_barrier
	s_setprio 1
	v_mfma_scale_f32_16x16x128_f8f6f4 v[88:91], v[26:33], v[182:189], 0, v177, v35 op_sel_hi:[0,0,0]
	v_mfma_scale_f32_16x16x128_f8f6f4 v[80:83], v[18:25], v[182:189], 0, v177, v35 op_sel_hi:[0,0,0]
	v_mfma_scale_f32_16x16x128_f8f6f4 v[72:75], v[26:33], v[190:197], 0, v177, v35 op_sel_hi:[0,0,0]
	v_mfma_scale_f32_16x16x128_f8f6f4 v[64:67], v[18:25], v[190:197], 0, v177, v35 op_sel_hi:[0,0,0]
	v_mfma_scale_f32_16x16x128_f8f6f4 v[56:59], v[26:33], v[198:205], 0, v177, v35 op_sel_hi:[0,0,0]
	v_mfma_scale_f32_16x16x128_f8f6f4 v[48:51], v[18:25], v[198:205], 0, v177, v35 op_sel_hi:[0,0,0]
	v_mfma_scale_f32_16x16x128_f8f6f4 v[40:43], v[26:33], v[218:225], 0, v177, v35 op_sel_hi:[0,0,0]
	v_mfma_scale_f32_16x16x128_f8f6f4 v[36:39], v[18:25], v[218:225], 0, v177, v35 op_sel_hi:[0,0,0]
	s_setprio 0
	s_add_i32 s82, 0, 0x18000
	v_add_u32_e32 v6, s82, v179
	s_barrier
	ds_read_b128 v[10:13], v6
	ds_read_b128 v[14:17], v6 offset:1024
	ds_read_b128 v[2:5], v6 offset:2048
	ds_read_b128 v[6:9], v6 offset:3072
	s_mov_b32 m0, s57
	ds_read_b128 v[18:21], v181 offset:32768
	ds_read_b128 v[22:25], v181 offset:33792
	ds_read_b128 v[26:29], v181 offset:34816
	ds_read_b128 v[30:33], v181 offset:35840
	ds_read_b128 v[182:185], v181 offset:36864
	ds_read_b128 v[186:189], v181 offset:37888
	ds_read_b128 v[190:193], v181 offset:38912
	ds_read_b128 v[194:197], v181 offset:39936
	s_nop 0
	v_lshl_add_u64 v[198:199], s[44:45], 0, v[172:173]
	global_load_lds_dwordx4 v[198:199], off
	v_lshl_add_u64 v[198:199], s[44:45], 0, v[174:175]
	s_mov_b32 m0, s58
	s_nop 0
	global_load_lds_dwordx4 v[198:199], off
	s_waitcnt lgkmcnt(8)
	s_barrier
	s_waitcnt lgkmcnt(0)
	s_setprio 1
	s_waitcnt lgkmcnt(0)
	v_mfma_scale_f32_16x16x128_f8f6f4 v[160:163], v[10:17], v[18:25], v[160:163], v176, v35 op_sel_hi:[0,0,0]
	v_mfma_scale_f32_16x16x128_f8f6f4 v[156:159], v[2:9], v[18:25], v[156:159], v176, v35 op_sel_hi:[0,0,0]
	v_mfma_scale_f32_16x16x128_f8f6f4 v[148:151], v[10:17], v[26:33], v[148:151], v176, v35 op_sel_hi:[0,0,0]
	v_mfma_scale_f32_16x16x128_f8f6f4 v[140:143], v[2:9], v[26:33], v[140:143], v176, v35 op_sel_hi:[0,0,0]
	v_mfma_scale_f32_16x16x128_f8f6f4 v[132:135], v[10:17], v[182:189], v[132:135], v176, v35 op_sel_hi:[0,0,0]
	v_mfma_scale_f32_16x16x128_f8f6f4 v[124:127], v[2:9], v[182:189], v[124:127], v176, v35 op_sel_hi:[0,0,0]
	v_mfma_scale_f32_16x16x128_f8f6f4 v[116:119], v[10:17], v[190:197], v[116:119], v176, v35 op_sel_hi:[0,0,0]
	v_mfma_scale_f32_16x16x128_f8f6f4 v[108:111], v[2:9], v[190:197], v[108:111], v176, v35 op_sel_hi:[0,0,0]
	s_setprio 0
	s_barrier
	s_add_i32 s83, 0, 0x1c000
	s_add_u32 s44, s40, 0x80
	v_add_u32_e32 v206, s83, v179
	s_addc_u32 s45, s41, 0
	s_add_i32 s82, s82, s17
	ds_read_b128 v[198:201], v206
	ds_read_b128 v[202:205], v206 offset:1024
	ds_read_b128 v[218:221], v206 offset:2048
	ds_read_b128 v[222:225], v206 offset:3072
	s_mov_b32 m0, s82
	v_lshl_add_u64 v[206:207], s[44:45], 0, v[166:167]
	global_load_lds_dwordx4 v[206:207], off
	v_lshl_add_u64 v[206:207], s[44:45], 0, v[164:165]
	s_add_i32 m0, s82, 0x2000
	s_nop 0
	global_load_lds_dwordx4 v[206:207], off
	s_barrier
	s_waitcnt lgkmcnt(0)
	s_setprio 1
	s_waitcnt lgkmcnt(0)
	v_mfma_scale_f32_16x16x128_f8f6f4 v[152:155], v[198:205], v[18:25], v[152:155], v177, v35 op_sel_hi:[0,0,0]
	v_mfma_scale_f32_16x16x128_f8f6f4 v[144:147], v[218:225], v[18:25], v[144:147], v177, v35 op_sel_hi:[0,0,0]
	v_mfma_scale_f32_16x16x128_f8f6f4 v[136:139], v[198:205], v[26:33], v[136:139], v177, v35 op_sel_hi:[0,0,0]
	v_mfma_scale_f32_16x16x128_f8f6f4 v[128:131], v[218:225], v[26:33], v[128:131], v177, v35 op_sel_hi:[0,0,0]
	v_mfma_scale_f32_16x16x128_f8f6f4 v[120:123], v[198:205], v[182:189], v[120:123], v177, v35 op_sel_hi:[0,0,0]
	v_mfma_scale_f32_16x16x128_f8f6f4 v[112:115], v[218:225], v[182:189], v[112:115], v177, v35 op_sel_hi:[0,0,0]
	v_mfma_scale_f32_16x16x128_f8f6f4 v[104:107], v[198:205], v[190:197], v[104:107], v177, v35 op_sel_hi:[0,0,0]
	v_mfma_scale_f32_16x16x128_f8f6f4 v[100:103], v[218:225], v[190:197], v[100:103], v177, v35 op_sel_hi:[0,0,0]
	s_setprio 0
	s_mov_b32 m0, s65
	s_barrier
	ds_read_b128 v[18:21], v181 offset:49152
	ds_read_b128 v[22:25], v181 offset:50176
	ds_read_b128 v[26:29], v181 offset:51200
	ds_read_b128 v[30:33], v181 offset:52224
	ds_read_b128 v[182:185], v181 offset:53248
	ds_read_b128 v[186:189], v181 offset:54272
	ds_read_b128 v[190:193], v181 offset:55296
	ds_read_b128 v[194:197], v181 offset:56320
	s_nop 0
	v_lshl_add_u64 v[206:207], s[42:43], 0, v[168:169]
	global_load_lds_dwordx4 v[206:207], off
	v_lshl_add_u64 v[206:207], s[42:43], 0, v[170:171]
	s_mov_b32 m0, s71
	s_nop 0
	global_load_lds_dwordx4 v[206:207], off
	s_barrier
	s_waitcnt lgkmcnt(0)
	s_setprio 1
	s_waitcnt lgkmcnt(0)
	v_mfma_scale_f32_16x16x128_f8f6f4 v[96:99], v[10:17], v[18:25], v[96:99], v176, v35 op_sel_hi:[0,0,0]
	v_mfma_scale_f32_16x16x128_f8f6f4 v[92:95], v[2:9], v[18:25], v[92:95], v176, v35 op_sel_hi:[0,0,0]
	v_mfma_scale_f32_16x16x128_f8f6f4 v[84:87], v[10:17], v[26:33], v[84:87], v176, v35 op_sel_hi:[0,0,0]
	v_mfma_scale_f32_16x16x128_f8f6f4 v[76:79], v[2:9], v[26:33], v[76:79], v176, v35 op_sel_hi:[0,0,0]
	v_mfma_scale_f32_16x16x128_f8f6f4 v[68:71], v[10:17], v[182:189], v[68:71], v176, v35 op_sel_hi:[0,0,0]
	v_mfma_scale_f32_16x16x128_f8f6f4 v[60:63], v[2:9], v[182:189], v[60:63], v176, v35 op_sel_hi:[0,0,0]
	v_mfma_scale_f32_16x16x128_f8f6f4 v[52:55], v[10:17], v[190:197], v[52:55], v176, v35 op_sel_hi:[0,0,0]
	v_mfma_scale_f32_16x16x128_f8f6f4 v[44:47], v[2:9], v[190:197], v[44:47], v176, v35 op_sel_hi:[0,0,0]
	s_setprio 0
	s_barrier
	s_add_u32 s40, s40, 0x20080
	s_addc_u32 s41, s41, 0
	s_add_i32 s42, s83, s17
	s_mov_b32 m0, s42
	v_lshl_add_u64 v[2:3], s[40:41], 0, v[166:167]
	global_load_lds_dwordx4 v[2:3], off
	v_lshl_add_u64 v[2:3], s[40:41], 0, v[164:165]
	s_add_i32 m0, s42, 0x2000
	s_nop 0
	global_load_lds_dwordx4 v[2:3], off
	s_waitcnt vmcnt(6)
	s_barrier
	s_setprio 1
	v_mfma_scale_f32_16x16x128_f8f6f4 v[88:91], v[198:205], v[18:25], v[88:91], v177, v35 op_sel_hi:[0,0,0]
	v_mfma_scale_f32_16x16x128_f8f6f4 v[80:83], v[218:225], v[18:25], v[80:83], v177, v35 op_sel_hi:[0,0,0]
	v_mfma_scale_f32_16x16x128_f8f6f4 v[72:75], v[198:205], v[26:33], v[72:75], v177, v35 op_sel_hi:[0,0,0]
	v_mfma_scale_f32_16x16x128_f8f6f4 v[64:67], v[218:225], v[26:33], v[64:67], v177, v35 op_sel_hi:[0,0,0]
	v_mfma_scale_f32_16x16x128_f8f6f4 v[56:59], v[198:205], v[182:189], v[56:59], v177, v35 op_sel_hi:[0,0,0]
	v_mfma_scale_f32_16x16x128_f8f6f4 v[48:51], v[218:225], v[182:189], v[48:51], v177, v35 op_sel_hi:[0,0,0]
	v_mfma_scale_f32_16x16x128_f8f6f4 v[40:43], v[198:205], v[190:197], v[40:43], v177, v35 op_sel_hi:[0,0,0]
	v_mfma_scale_f32_16x16x128_f8f6f4 v[36:39], v[218:225], v[190:197], v[36:39], v177, v35 op_sel_hi:[0,0,0]
	s_setprio 0
	s_add_i32 s81, s81, 2
	s_add_u32 s0, s0, 0x100
	s_addc_u32 s1, s1, 0
	s_add_u32 s79, s79, 0x100
	s_addc_u32 s80, s80, 0
	s_add_u32 s36, s36, 0x100
	s_addc_u32 s37, s37, 0
	s_cmp_gt_u32 s81, 5
	s_barrier
	s_cbranch_scc0 .LBB0_996
	s_branch .Lpeel_exit_1

.Lpeel_exit_1:
	s_lshl_b32 s0, s78, 8
	s_add_i32 s41, s0, s13
	s_cmpk_lt_i32 s41, 0x2000
	s_cselect_b64 s[0:1], -1, 0
	s_add_i32 s36, s41, 0xffffe000
	s_lshr_b32 s42, s36, 11
	s_and_b64 s[36:37], s[0:1], exec
	s_cselect_b32 s36, 32, s42
	s_ashr_i32 s37, s41, 31
	s_and_b64 s[0:1], s[0:1], exec
	s_cselect_b32 s1, s37, 0
	s_cselect_b32 s0, s41, s41
	s_lshl_b64 s[0:1], s[0:1], 11
	s_mul_hi_u32 s37, s36, 0x6000
	s_mulk_i32 s36, 0x6000
	s_add_u32 s36, s63, s36
	s_addc_u32 s37, s64, s37
	s_nop 7
	s_nop 7
	s_nop 3
	s_mov_b32 s40, 0
	v_lshl_or_b32 v18, s77, 8, v180
	s_add_u32 s0, s59, s0
	v_add_u32_e32 v20, s40, v178
	v_ashrrev_i32_e32 v19, 31, v18
	s_addc_u32 s1, s62, s1
	v_ashrrev_i32_e32 v21, 31, v20
	v_lshl_add_u64 v[6:7], v[18:19], 2, s[36:37]
	v_lshl_add_u64 v[18:19], v[18:19], 1, s[0:1]
	v_lshlrev_b64 v[20:21], 11, v[20:21]
	v_lshl_add_u64 v[18:19], v[18:19], 0, v[20:21]
	s_mov_b64 s[0:1], 0x8000
	v_lshl_add_u64 v[202:203], v[18:19], 0, s[0:1]
	s_mov_b32 s0, 0x8000
	v_add_co_u32_e32 v204, vcc, s0, v18
	s_mov_b64 s[0:1], 0x10000
	s_nop 0
	v_addc_co_u32_e32 v205, vcc, 0, v19, vcc
	v_lshl_add_u64 v[206:207], v[18:19], 0, s[0:1]
	s_mov_b32 s0, 0x10000
	v_add_co_u32_e32 v208, vcc, s0, v18
	s_mov_b64 s[0:1], 0x18000
	s_nop 0
	v_addc_co_u32_e32 v209, vcc, 0, v19, vcc
	v_lshl_add_u64 v[20:21], v[18:19], 0, s[0:1]
	s_mov_b32 s0, 0x18000
	global_load_dwordx4 v[10:13], v[6:7], off offset:16
	global_load_dwordx4 v[14:17], v[6:7], off
	global_load_dwordx4 v[2:5], v[6:7], off offset:528
	s_nop 0
	global_load_dwordx4 v[6:9], v[6:7], off offset:512
	v_add_co_u32_e32 v210, vcc, s0, v18
	global_load_dwordx4 v[22:25], v[18:19], off
	global_load_dwordx4 v[26:29], v[18:19], off offset:256
	v_addc_co_u32_e32 v211, vcc, 0, v19, vcc
	global_load_dwordx4 v[30:33], v[204:205], off
	global_load_dwordx4 v[182:185], v[202:203], off offset:256
	global_load_dwordx4 v[186:189], v[208:209], off
	global_load_dwordx4 v[190:193], v[206:207], off offset:256
	global_load_dwordx4 v[194:197], v[210:211], off
	global_load_dwordx4 v[198:201], v[20:21], off offset:256
	s_waitcnt vmcnt(0)
	v_lshlrev_b32_e32 v214, 16, v22
	v_and_b32_e32 v215, 0xffff0000, v22
	v_lshlrev_b32_e32 v22, 16, v23
	v_and_b32_e32 v23, 0xffff0000, v23
	v_lshlrev_b32_e32 v218, 16, v24
	v_and_b32_e32 v219, 0xffff0000, v24
	v_lshlrev_b32_e32 v24, 16, v25
	v_and_b32_e32 v25, 0xffff0000, v25
	v_pk_fma_f32 v[162:163], v[162:163], v[16:17], v[22:23]
	v_pk_fma_f32 v[22:23], v[160:161], v[14:15], v[214:215]
	v_pk_fma_f32 v[158:159], v[158:159], v[12:13], v[24:25]
	v_pk_fma_f32 v[24:25], v[156:157], v[10:11], v[218:219]
	v_cvt_pk_bf16_f32 v22, v22, v23
	v_cvt_pk_bf16_f32 v23, v162, v163
	v_cvt_pk_bf16_f32 v24, v24, v25
	v_cvt_pk_bf16_f32 v25, v158, v159
	global_store_dwordx4 v[18:19], v[22:25], off
	s_nop 1
	v_lshlrev_b32_e32 v22, 16, v26
	v_and_b32_e32 v23, 0xffff0000, v26
	v_lshlrev_b32_e32 v24, 16, v27
	v_and_b32_e32 v25, 0xffff0000, v27
	v_lshlrev_b32_e32 v26, 16, v28
	v_and_b32_e32 v27, 0xffff0000, v28
	v_lshlrev_b32_e32 v28, 16, v29
	v_and_b32_e32 v29, 0xffff0000, v29
	v_pk_fma_f32 v[24:25], v[154:155], v[8:9], v[24:25]
	v_pk_fma_f32 v[22:23], v[152:153], v[6:7], v[22:23]
	v_pk_fma_f32 v[28:29], v[146:147], v[4:5], v[28:29]
	v_pk_fma_f32 v[26:27], v[144:145], v[2:3], v[26:27]
	v_cvt_pk_bf16_f32 v22, v22, v23
	v_cvt_pk_bf16_f32 v23, v24, v25
	v_cvt_pk_bf16_f32 v24, v26, v27
	v_cvt_pk_bf16_f32 v25, v28, v29
	global_store_dwordx4 v[18:19], v[22:25], off offset:256
	v_lshlrev_b32_e32 v26, 16, v32
	v_and_b32_e32 v27, 0xffff0000, v32
	v_lshlrev_b32_e32 v22, 16, v30
	v_and_b32_e32 v23, 0xffff0000, v30
	v_lshlrev_b32_e32 v24, 16, v31
	v_and_b32_e32 v25, 0xffff0000, v31
	v_lshlrev_b32_e32 v28, 16, v33
	v_and_b32_e32 v29, 0xffff0000, v33
	v_pk_fma_f32 v[24:25], v[150:151], v[16:17], v[24:25]
	v_pk_fma_f32 v[22:23], v[148:149], v[14:15], v[22:23]
	v_pk_fma_f32 v[28:29], v[142:143], v[12:13], v[28:29]
	v_pk_fma_f32 v[26:27], v[140:141], v[10:11], v[26:27]
	v_cvt_pk_bf16_f32 v22, v22, v23
	v_cvt_pk_bf16_f32 v23, v24, v25
	v_cvt_pk_bf16_f32 v24, v26, v27
	v_cvt_pk_bf16_f32 v25, v28, v29
	global_store_dwordx4 v[204:205], v[22:25], off
	v_lshlrev_b32_e32 v26, 16, v184
	v_and_b32_e32 v27, 0xffff0000, v184
	v_lshlrev_b32_e32 v22, 16, v182
	v_and_b32_e32 v23, 0xffff0000, v182
	v_lshlrev_b32_e32 v24, 16, v183
	v_and_b32_e32 v25, 0xffff0000, v183
	v_lshlrev_b32_e32 v28, 16, v185
	v_and_b32_e32 v29, 0xffff0000, v185
	v_pk_fma_f32 v[24:25], v[138:139], v[8:9], v[24:25]
	v_pk_fma_f32 v[22:23], v[136:137], v[6:7], v[22:23]
	v_pk_fma_f32 v[28:29], v[130:131], v[4:5], v[28:29]
	v_pk_fma_f32 v[26:27], v[128:129], v[2:3], v[26:27]
	v_cvt_pk_bf16_f32 v22, v22, v23
	v_cvt_pk_bf16_f32 v23, v24, v25
	v_cvt_pk_bf16_f32 v24, v26, v27
	v_cvt_pk_bf16_f32 v25, v28, v29
	global_store_dwordx4 v[202:203], v[22:25], off offset:256
	v_lshlrev_b32_e32 v26, 16, v188
	v_and_b32_e32 v27, 0xffff0000, v188
	v_lshlrev_b32_e32 v22, 16, v186
	v_and_b32_e32 v23, 0xffff0000, v186
	v_lshlrev_b32_e32 v24, 16, v187
	v_and_b32_e32 v25, 0xffff0000, v187
	v_lshlrev_b32_e32 v28, 16, v189
	v_and_b32_e32 v29, 0xffff0000, v189
	v_pk_fma_f32 v[24:25], v[134:135], v[16:17], v[24:25]
	v_pk_fma_f32 v[22:23], v[132:133], v[14:15], v[22:23]
	v_pk_fma_f32 v[28:29], v[126:127], v[12:13], v[28:29]
	v_pk_fma_f32 v[26:27], v[124:125], v[10:11], v[26:27]
	v_cvt_pk_bf16_f32 v22, v22, v23
	v_cvt_pk_bf16_f32 v23, v24, v25
	v_cvt_pk_bf16_f32 v24, v26, v27
	v_cvt_pk_bf16_f32 v25, v28, v29
	global_store_dwordx4 v[208:209], v[22:25], off
	v_lshlrev_b32_e32 v26, 16, v192
	v_and_b32_e32 v27, 0xffff0000, v192
	v_lshlrev_b32_e32 v22, 16, v190
	v_and_b32_e32 v23, 0xffff0000, v190
	v_lshlrev_b32_e32 v24, 16, v191
	v_and_b32_e32 v25, 0xffff0000, v191
	v_lshlrev_b32_e32 v28, 16, v193
	v_and_b32_e32 v29, 0xffff0000, v193
	v_pk_fma_f32 v[24:25], v[122:123], v[8:9], v[24:25]
	v_pk_fma_f32 v[22:23], v[120:121], v[6:7], v[22:23]
	v_pk_fma_f32 v[28:29], v[114:115], v[4:5], v[28:29]
	v_pk_fma_f32 v[26:27], v[112:113], v[2:3], v[26:27]
	v_cvt_pk_bf16_f32 v22, v22, v23
	v_cvt_pk_bf16_f32 v23, v24, v25
	v_cvt_pk_bf16_f32 v24, v26, v27
	v_cvt_pk_bf16_f32 v25, v28, v29
	global_store_dwordx4 v[206:207], v[22:25], off offset:256
	v_lshlrev_b32_e32 v26, 16, v196
	v_and_b32_e32 v27, 0xffff0000, v196
	v_lshlrev_b32_e32 v22, 16, v194
	v_and_b32_e32 v23, 0xffff0000, v194
	v_lshlrev_b32_e32 v24, 16, v195
	v_and_b32_e32 v25, 0xffff0000, v195
	v_lshlrev_b32_e32 v28, 16, v197
	v_and_b32_e32 v29, 0xffff0000, v197
	v_pk_fma_f32 v[24:25], v[118:119], v[16:17], v[24:25]
	v_pk_fma_f32 v[22:23], v[116:117], v[14:15], v[22:23]
	v_pk_fma_f32 v[28:29], v[110:111], v[12:13], v[28:29]
	v_pk_fma_f32 v[26:27], v[108:109], v[10:11], v[26:27]
	v_cvt_pk_bf16_f32 v22, v22, v23
	v_cvt_pk_bf16_f32 v23, v24, v25
	v_cvt_pk_bf16_f32 v24, v26, v27
	v_cvt_pk_bf16_f32 v25, v28, v29
	global_store_dwordx4 v[210:211], v[22:25], off
	v_lshlrev_b32_e32 v26, 16, v200
	v_and_b32_e32 v27, 0xffff0000, v200
	v_lshlrev_b32_e32 v22, 16, v198
	v_and_b32_e32 v23, 0xffff0000, v198
	v_lshlrev_b32_e32 v24, 16, v199
	v_and_b32_e32 v25, 0xffff0000, v199
	v_lshlrev_b32_e32 v28, 16, v201
	v_and_b32_e32 v29, 0xffff0000, v201
	v_pk_fma_f32 v[24:25], v[106:107], v[8:9], v[24:25]
	v_pk_fma_f32 v[22:23], v[104:105], v[6:7], v[22:23]
	v_pk_fma_f32 v[28:29], v[102:103], v[4:5], v[28:29]
	v_pk_fma_f32 v[26:27], v[100:101], v[2:3], v[26:27]
	v_cvt_pk_bf16_f32 v22, v22, v23
	v_cvt_pk_bf16_f32 v23, v24, v25
	v_cvt_pk_bf16_f32 v24, v26, v27
	v_cvt_pk_bf16_f32 v25, v28, v29
	global_store_dwordx4 v[20:21], v[22:25], off offset:256
	s_mov_b64 s[0:1], 0x40000
	v_lshl_add_u64 v[120:121], v[18:19], 0, s[0:1]
	s_mov_b32 s0, 0x40000
	v_add_co_u32_e32 v122, vcc, s0, v18
	s_mov_b64 s[0:1], 0x48000
	s_nop 0
	v_addc_co_u32_e32 v123, vcc, 0, v19, vcc
	v_lshl_add_u64 v[124:125], v[18:19], 0, s[0:1]
	s_mov_b32 s0, 0x48000
	v_add_co_u32_e32 v126, vcc, s0, v18
	s_mov_b64 s[0:1], 0x50000
	s_nop 0
	v_addc_co_u32_e32 v127, vcc, 0, v19, vcc
	v_lshl_add_u64 v[128:129], v[18:19], 0, s[0:1]
	s_mov_b32 s0, 0x50000
	v_add_co_u32_e32 v130, vcc, s0, v18
	s_mov_b64 s[0:1], 0x58000
	s_nop 0
	v_addc_co_u32_e32 v131, vcc, 0, v19, vcc
	v_lshl_add_u64 v[20:21], v[18:19], 0, s[0:1]
	s_mov_b32 s0, 0x58000
	v_add_co_u32_e32 v18, vcc, s0, v18
	global_load_dwordx4 v[22:25], v[122:123], off
	global_load_dwordx4 v[26:29], v[120:121], off offset:256
	v_addc_co_u32_e32 v19, vcc, 0, v19, vcc
	global_load_dwordx4 v[30:33], v[126:127], off
	global_load_dwordx4 v[100:103], v[124:125], off offset:256
	global_load_dwordx4 v[104:107], v[130:131], off
	global_load_dwordx4 v[108:111], v[128:129], off offset:256
	global_load_dwordx4 v[112:115], v[18:19], off
	global_load_dwordx4 v[116:119], v[20:21], off offset:256
	s_waitcnt vmcnt(0)
	v_lshlrev_b32_e32 v132, 16, v22
	v_and_b32_e32 v133, 0xffff0000, v22
	v_lshlrev_b32_e32 v22, 16, v23
	v_and_b32_e32 v23, 0xffff0000, v23
	v_lshlrev_b32_e32 v134, 16, v24
	v_and_b32_e32 v135, 0xffff0000, v24
	v_lshlrev_b32_e32 v24, 16, v25
	v_and_b32_e32 v25, 0xffff0000, v25
	v_pk_fma_f32 v[98:99], v[98:99], v[16:17], v[22:23]
	v_pk_fma_f32 v[22:23], v[96:97], v[14:15], v[132:133]
	v_pk_fma_f32 v[94:95], v[94:95], v[12:13], v[24:25]
	v_pk_fma_f32 v[24:25], v[92:93], v[10:11], v[134:135]
	v_cvt_pk_bf16_f32 v22, v22, v23
	v_cvt_pk_bf16_f32 v23, v98, v99
	v_cvt_pk_bf16_f32 v24, v24, v25
	v_cvt_pk_bf16_f32 v25, v94, v95
	global_store_dwordx4 v[122:123], v[22:25], off
	s_nop 1
	v_lshlrev_b32_e32 v22, 16, v26
	v_and_b32_e32 v23, 0xffff0000, v26
	v_lshlrev_b32_e32 v24, 16, v27
	v_and_b32_e32 v25, 0xffff0000, v27
	v_lshlrev_b32_e32 v26, 16, v28
	v_and_b32_e32 v27, 0xffff0000, v28
	v_lshlrev_b32_e32 v28, 16, v29
	v_and_b32_e32 v29, 0xffff0000, v29
	v_pk_fma_f32 v[24:25], v[90:91], v[8:9], v[24:25]
	v_pk_fma_f32 v[22:23], v[88:89], v[6:7], v[22:23]
	v_pk_fma_f32 v[28:29], v[82:83], v[4:5], v[28:29]
	v_pk_fma_f32 v[26:27], v[80:81], v[2:3], v[26:27]
	v_cvt_pk_bf16_f32 v22, v22, v23
	v_cvt_pk_bf16_f32 v23, v24, v25
	v_cvt_pk_bf16_f32 v24, v26, v27
	v_cvt_pk_bf16_f32 v25, v28, v29
	global_store_dwordx4 v[120:121], v[22:25], off offset:256
	v_lshlrev_b32_e32 v26, 16, v32
	v_and_b32_e32 v27, 0xffff0000, v32
	v_lshlrev_b32_e32 v22, 16, v30
	v_and_b32_e32 v23, 0xffff0000, v30
	v_lshlrev_b32_e32 v24, 16, v31
	v_and_b32_e32 v25, 0xffff0000, v31
	v_lshlrev_b32_e32 v28, 16, v33
	v_and_b32_e32 v29, 0xffff0000, v33
	v_pk_fma_f32 v[24:25], v[86:87], v[16:17], v[24:25]
	v_pk_fma_f32 v[22:23], v[84:85], v[14:15], v[22:23]
	v_pk_fma_f32 v[28:29], v[78:79], v[12:13], v[28:29]
	v_pk_fma_f32 v[26:27], v[76:77], v[10:11], v[26:27]
	v_cvt_pk_bf16_f32 v22, v22, v23
	v_cvt_pk_bf16_f32 v23, v24, v25
	v_cvt_pk_bf16_f32 v24, v26, v27
	v_cvt_pk_bf16_f32 v25, v28, v29
	global_store_dwordx4 v[126:127], v[22:25], off
	v_lshlrev_b32_e32 v26, 16, v102
	v_and_b32_e32 v27, 0xffff0000, v102
	v_lshlrev_b32_e32 v22, 16, v100
	v_and_b32_e32 v23, 0xffff0000, v100
	v_lshlrev_b32_e32 v24, 16, v101
	v_and_b32_e32 v25, 0xffff0000, v101
	v_lshlrev_b32_e32 v28, 16, v103
	v_and_b32_e32 v29, 0xffff0000, v103
	v_pk_fma_f32 v[24:25], v[74:75], v[8:9], v[24:25]
	v_pk_fma_f32 v[22:23], v[72:73], v[6:7], v[22:23]
	v_pk_fma_f32 v[28:29], v[66:67], v[4:5], v[28:29]
	v_pk_fma_f32 v[26:27], v[64:65], v[2:3], v[26:27]
	v_cvt_pk_bf16_f32 v22, v22, v23
	v_cvt_pk_bf16_f32 v23, v24, v25
	v_cvt_pk_bf16_f32 v24, v26, v27
	v_cvt_pk_bf16_f32 v25, v28, v29
	global_store_dwordx4 v[124:125], v[22:25], off offset:256
	v_lshlrev_b32_e32 v26, 16, v106
	v_and_b32_e32 v27, 0xffff0000, v106
	v_lshlrev_b32_e32 v22, 16, v104
	v_and_b32_e32 v23, 0xffff0000, v104
	v_lshlrev_b32_e32 v24, 16, v105
	v_and_b32_e32 v25, 0xffff0000, v105
	v_lshlrev_b32_e32 v28, 16, v107
	v_and_b32_e32 v29, 0xffff0000, v107
	v_pk_fma_f32 v[24:25], v[70:71], v[16:17], v[24:25]
	v_pk_fma_f32 v[22:23], v[68:69], v[14:15], v[22:23]
	v_pk_fma_f32 v[28:29], v[62:63], v[12:13], v[28:29]
	v_pk_fma_f32 v[26:27], v[60:61], v[10:11], v[26:27]
	v_cvt_pk_bf16_f32 v22, v22, v23
	v_cvt_pk_bf16_f32 v23, v24, v25
	v_cvt_pk_bf16_f32 v24, v26, v27
	v_cvt_pk_bf16_f32 v25, v28, v29
	global_store_dwordx4 v[130:131], v[22:25], off
	v_lshlrev_b32_e32 v26, 16, v110
	v_and_b32_e32 v27, 0xffff0000, v110
	v_lshlrev_b32_e32 v22, 16, v108
	v_and_b32_e32 v23, 0xffff0000, v108
	v_lshlrev_b32_e32 v24, 16, v109
	v_and_b32_e32 v25, 0xffff0000, v109
	v_lshlrev_b32_e32 v28, 16, v111
	v_and_b32_e32 v29, 0xffff0000, v111
	v_pk_fma_f32 v[24:25], v[58:59], v[8:9], v[24:25]
	v_pk_fma_f32 v[22:23], v[56:57], v[6:7], v[22:23]
	v_pk_fma_f32 v[28:29], v[50:51], v[4:5], v[28:29]
	v_pk_fma_f32 v[26:27], v[48:49], v[2:3], v[26:27]
	v_cvt_pk_bf16_f32 v22, v22, v23
	v_cvt_pk_bf16_f32 v23, v24, v25
	v_cvt_pk_bf16_f32 v24, v26, v27
	v_cvt_pk_bf16_f32 v25, v28, v29
	global_store_dwordx4 v[128:129], v[22:25], off offset:256
	v_lshlrev_b32_e32 v26, 16, v114
	v_and_b32_e32 v27, 0xffff0000, v114
	v_lshlrev_b32_e32 v22, 16, v112
	v_and_b32_e32 v23, 0xffff0000, v112
	v_lshlrev_b32_e32 v24, 16, v113
	v_and_b32_e32 v25, 0xffff0000, v113
	v_lshlrev_b32_e32 v28, 16, v115
	v_and_b32_e32 v29, 0xffff0000, v115
	v_pk_fma_f32 v[16:17], v[54:55], v[16:17], v[24:25]
	v_pk_fma_f32 v[14:15], v[52:53], v[14:15], v[22:23]
	v_pk_fma_f32 v[22:23], v[46:47], v[12:13], v[28:29]
	v_pk_fma_f32 v[12:13], v[44:45], v[10:11], v[26:27]
	v_cvt_pk_bf16_f32 v10, v14, v15
	v_cvt_pk_bf16_f32 v11, v16, v17
	v_cvt_pk_bf16_f32 v12, v12, v13
	v_cvt_pk_bf16_f32 v13, v22, v23
	global_store_dwordx4 v[18:19], v[10:13], off
	v_lshlrev_b32_e32 v14, 16, v118
	v_and_b32_e32 v15, 0xffff0000, v118
	v_lshlrev_b32_e32 v10, 16, v116
	v_and_b32_e32 v11, 0xffff0000, v116
	v_lshlrev_b32_e32 v12, 16, v117
	v_and_b32_e32 v13, 0xffff0000, v117
	v_lshlrev_b32_e32 v16, 16, v119
	v_and_b32_e32 v17, 0xffff0000, v119
	v_pk_fma_f32 v[8:9], v[42:43], v[8:9], v[12:13]
	v_pk_fma_f32 v[6:7], v[40:41], v[6:7], v[10:11]
	v_pk_fma_f32 v[10:11], v[38:39], v[4:5], v[16:17]
	v_pk_fma_f32 v[4:5], v[36:37], v[2:3], v[14:15]
	v_cvt_pk_bf16_f32 v2, v6, v7
	v_cvt_pk_bf16_f32 v3, v8, v9
	v_cvt_pk_bf16_f32 v4, v4, v5
	v_cvt_pk_bf16_f32 v5, v10, v11
	global_store_dwordx4 v[20:21], v[2:5], off offset:256
	s_and_b64 vcc, exec, s[38:39]
	s_mov_b32 s77, s73
	s_mov_b32 s78, s76
	s_mov_b64 s[40:41], s[18:19]
	s_mov_b64 s[36:37], s[2:3]
	s_cbranch_vccz .LBB0_993
	s_waitcnt vmcnt(0)
	v_readlane_b32 s64, v255, 32
	v_readlane_b32 s72, v255, 34
	s_cmpk_gt_u32 s14, 0xff
	v_readlane_b32 s65, v255, 33
	v_readlane_b32 s73, v255, 35
	v_readlane_b32 s71, v255, 36
	s_cbranch_scc1 .LBB0_1000
	s_barrier

.LBB0_1010:
	s_add_u32 s0, s44, 0x100
	s_addc_u32 s1, s45, 0
	s_add_u32 s20, s46, 0x100
	s_addc_u32 s85, s47, 0
	s_add_u32 s44, s44, 0x80
	s_addc_u32 s45, s45, 0
	s_mov_b32 s86, -2
	s_cmp_eq_u32 s86, 12
	s_cselect_b32 s14, s40, s0
	s_cselect_b32 s15, s41, s1
	s_cselect_b32 s46, s42, s20
	s_cselect_b32 s47, s43, s85
	s_add_u32 s48, s14, 0x80
	s_addc_u32 s49, s15, 0
	s_add_i32 s87, 0, 0x10000
	s_waitcnt vmcnt(0)
	v_add_u32_e32 v144, s87, v170
	ds_read_b128 v[132:135], v144
	ds_read_b128 v[136:139], v144 offset:1024
	ds_read_b128 v[140:143], v144 offset:2048
	ds_read_b128 v[144:147], v144 offset:3072
	s_mov_b64 s[88:89], s[44:45]
	ds_read_b128 v[160:163], v172
	ds_read_b128 v[164:167], v172 offset:1024
	ds_read_b128 v[174:177], v172 offset:2048
	ds_read_b128 v[178:181], v172 offset:3072
	ds_read_b128 v[182:185], v172 offset:4096
	ds_read_b128 v[186:189], v172 offset:5120
	ds_read_b128 v[190:193], v172 offset:6144
	ds_read_b128 v[194:197], v172 offset:7168
	s_add_i32 m0, s63, 0xc000
	v_lshl_add_u64 v[168:169], s[88:89], 0, v[156:157]
	global_load_lds_dwordx4 v[168:169], off
	v_lshl_add_u64 v[168:169], s[88:89], 0, v[158:159]
	s_add_i32 m0, s63, 0xe000
	s_nop 0
	global_load_lds_dwordx4 v[168:169], off
	s_waitcnt lgkmcnt(8)
	s_barrier
	s_waitcnt lgkmcnt(0)
	s_setprio 1
	s_waitcnt lgkmcnt(0)
	v_mfma_f32_16x16x32_bf16 v[128:131], v[132:135], v[160:163], 0
	v_mfma_f32_16x16x32_bf16 v[124:127], v[140:143], v[160:163], 0
	v_mfma_f32_16x16x32_bf16 v[116:119], v[132:135], v[174:177], 0
	v_mfma_f32_16x16x32_bf16 v[108:111], v[140:143], v[174:177], 0
	v_mfma_f32_16x16x32_bf16 v[96:99], v[132:135], v[182:185], 0
	v_mfma_f32_16x16x32_bf16 v[92:95], v[140:143], v[182:185], 0
	v_mfma_f32_16x16x32_bf16 v[84:87], v[132:135], v[190:193], 0
	v_mfma_f32_16x16x32_bf16 v[76:79], v[140:143], v[190:193], 0
	v_mfma_f32_16x16x32_bf16 v[128:131], v[136:139], v[164:167], v[128:131]
	v_mfma_f32_16x16x32_bf16 v[124:127], v[144:147], v[164:167], v[124:127]
	v_mfma_f32_16x16x32_bf16 v[116:119], v[136:139], v[178:181], v[116:119]
	v_mfma_f32_16x16x32_bf16 v[108:111], v[144:147], v[178:181], v[108:111]
	v_mfma_f32_16x16x32_bf16 v[96:99], v[136:139], v[186:189], v[96:99]
	v_mfma_f32_16x16x32_bf16 v[92:95], v[144:147], v[186:189], v[92:95]
	v_mfma_f32_16x16x32_bf16 v[84:87], v[136:139], v[194:197], v[84:87]
	v_mfma_f32_16x16x32_bf16 v[76:79], v[144:147], v[194:197], v[76:79]
	s_setprio 0
	s_barrier
	s_add_i32 s90, 0, 0x14000
	v_add_u32_e32 v168, s90, v170
	s_mov_b64 s[88:89], s[46:47]
	s_add_i32 s87, s87, s57
	ds_read_b128 v[198:201], v168
	ds_read_b128 v[202:205], v168 offset:1024
	ds_read_b128 v[206:209], v168 offset:2048
	ds_read_b128 v[218:221], v168 offset:3072
	s_mov_b32 m0, s87
	v_lshl_add_u64 v[168:169], s[88:89], 0, v[150:151]
	global_load_lds_dwordx4 v[168:169], off
	v_lshl_add_u64 v[168:169], s[88:89], 0, v[148:149]
	s_add_i32 m0, s87, 0x2000
	s_nop 0
	global_load_lds_dwordx4 v[168:169], off
	s_barrier
	s_waitcnt lgkmcnt(0)
	s_setprio 1
	s_waitcnt lgkmcnt(0)
	v_mfma_f32_16x16x32_bf16 v[120:123], v[198:201], v[160:163], 0
	v_mfma_f32_16x16x32_bf16 v[112:115], v[206:209], v[160:163], 0
	v_mfma_f32_16x16x32_bf16 v[104:107], v[198:201], v[174:177], 0
	v_mfma_f32_16x16x32_bf16 v[100:103], v[206:209], v[174:177], 0
	v_mfma_f32_16x16x32_bf16 v[88:91], v[198:201], v[182:185], 0
	v_mfma_f32_16x16x32_bf16 v[80:83], v[206:209], v[182:185], 0
	v_mfma_f32_16x16x32_bf16 v[72:75], v[198:201], v[190:193], 0
	v_mfma_f32_16x16x32_bf16 v[68:71], v[206:209], v[190:193], 0
	v_mfma_f32_16x16x32_bf16 v[120:123], v[202:205], v[164:167], v[120:123]
	v_mfma_f32_16x16x32_bf16 v[112:115], v[218:221], v[164:167], v[112:115]
	v_mfma_f32_16x16x32_bf16 v[104:107], v[202:205], v[178:181], v[104:107]
	v_mfma_f32_16x16x32_bf16 v[100:103], v[218:221], v[178:181], v[100:103]
	v_mfma_f32_16x16x32_bf16 v[88:91], v[202:205], v[186:189], v[88:91]
	v_mfma_f32_16x16x32_bf16 v[80:83], v[218:221], v[186:189], v[80:83]
	v_mfma_f32_16x16x32_bf16 v[72:75], v[202:205], v[194:197], v[72:75]
	v_mfma_f32_16x16x32_bf16 v[68:71], v[218:221], v[194:197], v[68:71]
	s_setprio 0
	s_mov_b64 s[88:89], s[14:15]
	s_mov_b32 m0, s63
	s_barrier
	ds_read_b128 v[160:163], v172 offset:16384
	ds_read_b128 v[164:167], v172 offset:17408
	ds_read_b128 v[174:177], v172 offset:18432
	ds_read_b128 v[178:181], v172 offset:19456
	ds_read_b128 v[182:185], v172 offset:20480
	ds_read_b128 v[186:189], v172 offset:21504
	ds_read_b128 v[190:193], v172 offset:22528
	ds_read_b128 v[194:197], v172 offset:23552
	s_nop 0
	v_lshl_add_u64 v[168:169], s[88:89], 0, v[152:153]
	global_load_lds_dwordx4 v[168:169], off
	v_lshl_add_u64 v[168:169], s[88:89], 0, v[154:155]
	s_mov_b32 m0, s64
	s_nop 0
	global_load_lds_dwordx4 v[168:169], off
	s_barrier
	s_waitcnt lgkmcnt(0)
	s_setprio 1
	s_waitcnt lgkmcnt(0)
	v_mfma_f32_16x16x32_bf16 v[64:67], v[132:135], v[160:163], 0
	v_mfma_f32_16x16x32_bf16 v[60:63], v[140:143], v[160:163], 0
	v_mfma_f32_16x16x32_bf16 v[56:59], v[132:135], v[174:177], 0
	v_mfma_f32_16x16x32_bf16 v[48:51], v[140:143], v[174:177], 0
	v_mfma_f32_16x16x32_bf16 v[30:33], v[132:135], v[182:185], 0
	v_mfma_f32_16x16x32_bf16 v[26:29], v[140:143], v[182:185], 0
	v_mfma_f32_16x16x32_bf16 v[22:25], v[132:135], v[190:193], 0
	v_mfma_f32_16x16x32_bf16 v[14:17], v[140:143], v[190:193], 0
	v_mfma_f32_16x16x32_bf16 v[64:67], v[136:139], v[164:167], v[64:67]
	v_mfma_f32_16x16x32_bf16 v[60:63], v[144:147], v[164:167], v[60:63]
	v_mfma_f32_16x16x32_bf16 v[56:59], v[136:139], v[178:181], v[56:59]
	v_mfma_f32_16x16x32_bf16 v[48:51], v[144:147], v[178:181], v[48:51]
	v_mfma_f32_16x16x32_bf16 v[30:33], v[136:139], v[186:189], v[30:33]
	v_mfma_f32_16x16x32_bf16 v[26:29], v[144:147], v[186:189], v[26:29]
	v_mfma_f32_16x16x32_bf16 v[22:25], v[136:139], v[194:197], v[22:25]
	v_mfma_f32_16x16x32_bf16 v[14:17], v[144:147], v[194:197], v[14:17]
	s_setprio 0
	s_barrier
	s_add_u32 s88, s46, 0x40000
	s_addc_u32 s89, s47, 0
	s_add_i32 s87, s90, s57
	s_mov_b32 m0, s87
	v_lshl_add_u64 v[132:133], s[88:89], 0, v[150:151]
	global_load_lds_dwordx4 v[132:133], off
	v_lshl_add_u64 v[132:133], s[88:89], 0, v[148:149]
	s_add_i32 m0, s87, 0x2000
	s_nop 0
	global_load_lds_dwordx4 v[132:133], off
	s_waitcnt vmcnt(6)
	s_barrier
	s_setprio 1
	v_mfma_f32_16x16x32_bf16 v[52:55], v[198:201], v[160:163], 0
	v_mfma_f32_16x16x32_bf16 v[44:47], v[206:209], v[160:163], 0
	v_mfma_f32_16x16x32_bf16 v[40:43], v[198:201], v[174:177], 0
	v_mfma_f32_16x16x32_bf16 v[36:39], v[206:209], v[174:177], 0
	v_mfma_f32_16x16x32_bf16 v[18:21], v[198:201], v[182:185], 0
	v_mfma_f32_16x16x32_bf16 v[10:13], v[206:209], v[182:185], 0
	v_mfma_f32_16x16x32_bf16 v[6:9], v[198:201], v[190:193], 0
	v_mfma_f32_16x16x32_bf16 v[2:5], v[206:209], v[190:193], 0
	v_mfma_f32_16x16x32_bf16 v[52:55], v[202:205], v[164:167], v[52:55]
	v_mfma_f32_16x16x32_bf16 v[44:47], v[218:221], v[164:167], v[44:47]
	v_mfma_f32_16x16x32_bf16 v[40:43], v[202:205], v[178:181], v[40:43]
	v_mfma_f32_16x16x32_bf16 v[36:39], v[218:221], v[178:181], v[36:39]
	v_mfma_f32_16x16x32_bf16 v[18:21], v[202:205], v[186:189], v[18:21]
	v_mfma_f32_16x16x32_bf16 v[10:13], v[218:221], v[186:189], v[10:13]
	v_mfma_f32_16x16x32_bf16 v[6:9], v[202:205], v[194:197], v[6:9]
	v_mfma_f32_16x16x32_bf16 v[2:5], v[218:221], v[194:197], v[2:5]
	s_setprio 0
	s_add_i32 s87, 0, 0x18000
	v_add_u32_e32 v144, s87, v170
	s_barrier
	ds_read_b128 v[132:135], v144
	ds_read_b128 v[136:139], v144 offset:1024
	ds_read_b128 v[140:143], v144 offset:2048
	ds_read_b128 v[144:147], v144 offset:3072
	s_mov_b32 m0, s65
	ds_read_b128 v[160:163], v172 offset:32768
	ds_read_b128 v[164:167], v172 offset:33792
	ds_read_b128 v[174:177], v172 offset:34816
	ds_read_b128 v[178:181], v172 offset:35840
	ds_read_b128 v[182:185], v172 offset:36864
	ds_read_b128 v[186:189], v172 offset:37888
	ds_read_b128 v[190:193], v172 offset:38912
	ds_read_b128 v[194:197], v172 offset:39936
	s_nop 0
	v_lshl_add_u64 v[168:169], s[14:15], 0, v[156:157]
	global_load_lds_dwordx4 v[168:169], off
	v_lshl_add_u64 v[168:169], s[14:15], 0, v[158:159]
	s_mov_b32 m0, s71
	s_nop 0
	global_load_lds_dwordx4 v[168:169], off
	s_waitcnt lgkmcnt(8)
	s_barrier
	s_waitcnt lgkmcnt(0)
	s_setprio 1
	s_waitcnt lgkmcnt(0)
	v_mfma_f32_16x16x32_bf16 v[128:131], v[132:135], v[160:163], v[128:131]
	v_mfma_f32_16x16x32_bf16 v[124:127], v[140:143], v[160:163], v[124:127]
	v_mfma_f32_16x16x32_bf16 v[116:119], v[132:135], v[174:177], v[116:119]
	v_mfma_f32_16x16x32_bf16 v[108:111], v[140:143], v[174:177], v[108:111]
	v_mfma_f32_16x16x32_bf16 v[96:99], v[132:135], v[182:185], v[96:99]
	v_mfma_f32_16x16x32_bf16 v[92:95], v[140:143], v[182:185], v[92:95]
	v_mfma_f32_16x16x32_bf16 v[84:87], v[132:135], v[190:193], v[84:87]
	v_mfma_f32_16x16x32_bf16 v[76:79], v[140:143], v[190:193], v[76:79]
	v_mfma_f32_16x16x32_bf16 v[128:131], v[136:139], v[164:167], v[128:131]
	v_mfma_f32_16x16x32_bf16 v[124:127], v[144:147], v[164:167], v[124:127]
	v_mfma_f32_16x16x32_bf16 v[116:119], v[136:139], v[178:181], v[116:119]
	v_mfma_f32_16x16x32_bf16 v[108:111], v[144:147], v[178:181], v[108:111]
	v_mfma_f32_16x16x32_bf16 v[96:99], v[136:139], v[186:189], v[96:99]
	v_mfma_f32_16x16x32_bf16 v[92:95], v[144:147], v[186:189], v[92:95]
	v_mfma_f32_16x16x32_bf16 v[84:87], v[136:139], v[194:197], v[84:87]
	v_mfma_f32_16x16x32_bf16 v[76:79], v[144:147], v[194:197], v[76:79]
	s_setprio 0
	s_barrier
	s_add_i32 s88, 0, 0x1c000
	s_add_u32 s14, s46, 0x80
	v_add_u32_e32 v168, s88, v170
	s_addc_u32 s15, s47, 0
	s_add_i32 s87, s87, s57
	ds_read_b128 v[198:201], v168
	ds_read_b128 v[202:205], v168 offset:1024
	ds_read_b128 v[206:209], v168 offset:2048
	ds_read_b128 v[218:221], v168 offset:3072
	s_mov_b32 m0, s87
	v_lshl_add_u64 v[168:169], s[14:15], 0, v[150:151]
	global_load_lds_dwordx4 v[168:169], off
	v_lshl_add_u64 v[168:169], s[14:15], 0, v[148:149]
	s_add_i32 m0, s87, 0x2000
	s_nop 0
	global_load_lds_dwordx4 v[168:169], off
	s_barrier
	s_waitcnt lgkmcnt(0)
	s_setprio 1
	s_waitcnt lgkmcnt(0)
	v_mfma_f32_16x16x32_bf16 v[120:123], v[198:201], v[160:163], v[120:123]
	v_mfma_f32_16x16x32_bf16 v[112:115], v[206:209], v[160:163], v[112:115]
	v_mfma_f32_16x16x32_bf16 v[104:107], v[198:201], v[174:177], v[104:107]
	v_mfma_f32_16x16x32_bf16 v[100:103], v[206:209], v[174:177], v[100:103]
	v_mfma_f32_16x16x32_bf16 v[88:91], v[198:201], v[182:185], v[88:91]
	v_mfma_f32_16x16x32_bf16 v[80:83], v[206:209], v[182:185], v[80:83]
	v_mfma_f32_16x16x32_bf16 v[72:75], v[198:201], v[190:193], v[72:75]
	v_mfma_f32_16x16x32_bf16 v[68:71], v[206:209], v[190:193], v[68:71]
	v_mfma_f32_16x16x32_bf16 v[120:123], v[202:205], v[164:167], v[120:123]
	v_mfma_f32_16x16x32_bf16 v[112:115], v[218:221], v[164:167], v[112:115]
	v_mfma_f32_16x16x32_bf16 v[104:107], v[202:205], v[178:181], v[104:107]
	v_mfma_f32_16x16x32_bf16 v[100:103], v[218:221], v[178:181], v[100:103]
	v_mfma_f32_16x16x32_bf16 v[88:91], v[202:205], v[186:189], v[88:91]
	v_mfma_f32_16x16x32_bf16 v[80:83], v[218:221], v[186:189], v[80:83]
	v_mfma_f32_16x16x32_bf16 v[72:75], v[202:205], v[194:197], v[72:75]
	v_mfma_f32_16x16x32_bf16 v[68:71], v[218:221], v[194:197], v[68:71]
	s_setprio 0
	s_mov_b32 m0, s78
	s_barrier
	ds_read_b128 v[160:163], v172 offset:49152
	ds_read_b128 v[164:167], v172 offset:50176
	ds_read_b128 v[174:177], v172 offset:51200
	ds_read_b128 v[178:181], v172 offset:52224
	ds_read_b128 v[182:185], v172 offset:53248
	ds_read_b128 v[186:189], v172 offset:54272
	ds_read_b128 v[190:193], v172 offset:55296
	ds_read_b128 v[194:197], v172 offset:56320
	s_nop 0
	v_lshl_add_u64 v[168:169], s[48:49], 0, v[152:153]
	global_load_lds_dwordx4 v[168:169], off
	v_lshl_add_u64 v[168:169], s[48:49], 0, v[154:155]
	s_mov_b32 m0, s79
	s_nop 0
	global_load_lds_dwordx4 v[168:169], off
	s_barrier
	s_waitcnt lgkmcnt(0)
	s_setprio 1
	s_waitcnt lgkmcnt(0)
	v_mfma_f32_16x16x32_bf16 v[64:67], v[132:135], v[160:163], v[64:67]
	v_mfma_f32_16x16x32_bf16 v[60:63], v[140:143], v[160:163], v[60:63]
	v_mfma_f32_16x16x32_bf16 v[56:59], v[132:135], v[174:177], v[56:59]
	v_mfma_f32_16x16x32_bf16 v[48:51], v[140:143], v[174:177], v[48:51]
	v_mfma_f32_16x16x32_bf16 v[30:33], v[132:135], v[182:185], v[30:33]
	v_mfma_f32_16x16x32_bf16 v[26:29], v[140:143], v[182:185], v[26:29]
	v_mfma_f32_16x16x32_bf16 v[22:25], v[132:135], v[190:193], v[22:25]
	v_mfma_f32_16x16x32_bf16 v[14:17], v[140:143], v[190:193], v[14:17]
	v_mfma_f32_16x16x32_bf16 v[64:67], v[136:139], v[164:167], v[64:67]
	v_mfma_f32_16x16x32_bf16 v[60:63], v[144:147], v[164:167], v[60:63]
	v_mfma_f32_16x16x32_bf16 v[56:59], v[136:139], v[178:181], v[56:59]
	v_mfma_f32_16x16x32_bf16 v[48:51], v[144:147], v[178:181], v[48:51]
	v_mfma_f32_16x16x32_bf16 v[30:33], v[136:139], v[186:189], v[30:33]
	v_mfma_f32_16x16x32_bf16 v[26:29], v[144:147], v[186:189], v[26:29]
	v_mfma_f32_16x16x32_bf16 v[22:25], v[136:139], v[194:197], v[22:25]
	v_mfma_f32_16x16x32_bf16 v[14:17], v[144:147], v[194:197], v[14:17]
	s_setprio 0
	s_barrier
	s_add_u32 s14, s46, 0x40080
	s_addc_u32 s15, s47, 0
	s_add_i32 s46, s88, s57
	s_mov_b32 m0, s46
	v_lshl_add_u64 v[132:133], s[14:15], 0, v[150:151]
	global_load_lds_dwordx4 v[132:133], off
	v_lshl_add_u64 v[132:133], s[14:15], 0, v[148:149]
	s_add_i32 m0, s46, 0x2000
	s_nop 0
	global_load_lds_dwordx4 v[132:133], off
	s_waitcnt vmcnt(6)
	s_barrier
	s_setprio 1
	v_mfma_f32_16x16x32_bf16 v[52:55], v[198:201], v[160:163], v[52:55]
	v_mfma_f32_16x16x32_bf16 v[44:47], v[206:209], v[160:163], v[44:47]
	v_mfma_f32_16x16x32_bf16 v[40:43], v[198:201], v[174:177], v[40:43]
	v_mfma_f32_16x16x32_bf16 v[36:39], v[206:209], v[174:177], v[36:39]
	v_mfma_f32_16x16x32_bf16 v[18:21], v[198:201], v[182:185], v[18:21]
	v_mfma_f32_16x16x32_bf16 v[10:13], v[206:209], v[182:185], v[10:13]
	v_mfma_f32_16x16x32_bf16 v[6:9], v[198:201], v[190:193], v[6:9]
	v_mfma_f32_16x16x32_bf16 v[2:5], v[206:209], v[190:193], v[2:5]
	v_mfma_f32_16x16x32_bf16 v[52:55], v[202:205], v[164:167], v[52:55]
	v_mfma_f32_16x16x32_bf16 v[44:47], v[218:221], v[164:167], v[44:47]
	v_mfma_f32_16x16x32_bf16 v[40:43], v[202:205], v[178:181], v[40:43]
	v_mfma_f32_16x16x32_bf16 v[36:39], v[218:221], v[178:181], v[36:39]
	v_mfma_f32_16x16x32_bf16 v[18:21], v[202:205], v[186:189], v[18:21]
	v_mfma_f32_16x16x32_bf16 v[10:13], v[218:221], v[186:189], v[10:13]
	v_mfma_f32_16x16x32_bf16 v[6:9], v[202:205], v[194:197], v[6:9]
	v_mfma_f32_16x16x32_bf16 v[2:5], v[218:221], v[194:197], v[2:5]
	s_setprio 0
	s_add_i32 s86, s86, 2
	s_add_u32 s0, s0, 0x100
	s_addc_u32 s1, s1, 0
	s_add_u32 s20, s20, 0x100
	s_addc_u32 s85, s85, 0
	s_add_u32 s44, s44, 0x100
	s_addc_u32 s45, s45, 0
	s_cmp_gt_u32 s86, 13
	s_barrier
	s_cbranch_scc0 .LBB0_1011
	s_branch .Lpeel_exit_2

.Lpeel_exit_2:
	s_lshl_b32 s0, s84, 8
	s_add_i32 s0, s0, s13
	s_cmpk_lt_i32 s0, 0x2000
	s_cselect_b64 s[14:15], -1, 0
	s_add_i32 s20, s0, 0xffffe000
	s_cmpk_gt_i32 s0, 0x1fff
	s_mov_b64 s[46:47], -1
	s_mov_b32 s48, 0
	s_cbranch_scc0 .LBB0_1014
	s_lshl_b64 s[44:45], s[20:21], 12
	s_add_u32 s44, s18, s44
	s_addc_u32 s45, s19, s45
	s_mov_b32 s1, s21
	s_mov_b64 s[46:47], 0

.LBB0_1338:
	s_mov_b32 s0, 0
	s_mov_b64 s[46:47], -1
	s_mov_b64 s[48:49], 0
	s_add_u32 s19, s42, s0
	s_addc_u32 s52, s43, 0
	s_add_u32 s1, s19, 0x100
	s_addc_u32 s50, s52, 0
	s_and_b64 s[14:15], s[48:49], exec
	s_cselect_b32 s55, s29, s50
	s_cselect_b32 s54, s28, s1
	s_add_u32 s0, s44, s0
	s_addc_u32 s1, s45, 0
	s_add_u32 s14, s0, 0x100
	s_addc_u32 s15, s1, 0
	s_add_u32 s50, s54, 0x80
	s_addc_u32 s51, s55, 0
	s_add_i32 s92, 0, 0x10000
	s_and_b64 s[0:1], s[48:49], exec
	s_cselect_b32 s15, s37, s15
	s_cselect_b32 s14, s36, s14
	s_add_u32 s90, s19, 0x80
	s_addc_u32 s91, s52, 0
	s_add_i32 s95, s92, s76
	s_add_i32 m0, s41, 0xc000
	s_add_i32 s93, s41, 0xe000
	s_add_i32 s94, 0, 0x14000
	s_add_i32 vcc_lo, s95, 0x2000
	s_add_u32 s56, s14, 0x1000
	s_addc_u32 s57, s15, 0
	s_add_i32 s89, s94, s76
	v_add_u32_e32 v6, s92, v178
	s_add_i32 s88, s89, 0x2000
	s_add_i32 s87, 0, 0x18000
	s_add_i32 s85, 0, 0x1c000
	ds_read_b128 v[10:13], v6
	ds_read_b128 v[14:17], v6 offset:1024
	ds_read_b128 v[2:5], v6 offset:2048
	ds_read_b128 v[6:9], v6 offset:3072
	s_add_u32 s52, s14, 0x80
	s_addc_u32 s53, s15, 0
	s_add_i32 s86, s87, s76
	s_add_i32 s19, s86, 0x2000
	s_add_u32 s48, s14, 0x1080
	s_addc_u32 s49, s15, 0
	s_add_i32 s1, s85, s76
	s_add_i32 s0, s1, 0x2000
	ds_read_b128 v[182:185], v180
	ds_read_b128 v[186:189], v180 offset:1024
	ds_read_b128 v[190:193], v180 offset:2048
	ds_read_b128 v[194:197], v180 offset:3072
	ds_read_b128 v[198:201], v180 offset:4096
	ds_read_b128 v[202:205], v180 offset:5120
	ds_read_b128 v[218:221], v180 offset:6144
	ds_read_b128 v[222:225], v180 offset:7168
	s_nop 0
	v_lshl_add_u64 v[18:19], s[90:91], 0, v[172:173]
	global_load_lds_dwordx4 v[18:19], off
	v_lshl_add_u64 v[18:19], s[90:91], 0, v[174:175]
	s_mov_b32 m0, s93
	s_nop 0
	global_load_lds_dwordx4 v[18:19], off
	s_waitcnt lgkmcnt(8)
	s_barrier
	s_waitcnt lgkmcnt(0)
	s_setprio 1
	s_waitcnt lgkmcnt(0)
	v_mfma_scale_f32_16x16x128_f8f6f4 v[160:163], v[10:17], v[182:189], 0, v35, v1 op_sel_hi:[0,0,0]
	v_mfma_scale_f32_16x16x128_f8f6f4 v[156:159], v[2:9], v[182:189], 0, v35, v1 op_sel_hi:[0,0,0]
	v_mfma_scale_f32_16x16x128_f8f6f4 v[144:147], v[10:17], v[190:197], 0, v35, v1 op_sel_hi:[0,0,0]
	v_mfma_scale_f32_16x16x128_f8f6f4 v[140:143], v[2:9], v[190:197], 0, v35, v1 op_sel_hi:[0,0,0]
	v_mfma_scale_f32_16x16x128_f8f6f4 v[128:131], v[10:17], v[198:205], 0, v35, v1 op_sel_hi:[0,0,0]
	v_mfma_scale_f32_16x16x128_f8f6f4 v[124:127], v[2:9], v[198:205], 0, v35, v1 op_sel_hi:[0,0,0]
	v_mfma_scale_f32_16x16x128_f8f6f4 v[112:115], v[10:17], v[218:225], 0, v35, v1 op_sel_hi:[0,0,0]
	v_mfma_scale_f32_16x16x128_f8f6f4 v[108:111], v[2:9], v[218:225], 0, v35, v1 op_sel_hi:[0,0,0]
	s_setprio 0
	s_barrier
	v_add_u32_e32 v22, s94, v178
	s_mov_b32 m0, s95
	ds_read_b128 v[26:29], v22
	ds_read_b128 v[30:33], v22 offset:1024
	ds_read_b128 v[18:21], v22 offset:2048
	ds_read_b128 v[22:25], v22 offset:3072
	s_nop 0
	v_lshl_add_u64 v[206:207], s[14:15], 0, v[164:165]
	global_load_lds_dwordx4 v[206:207], off
	v_lshl_add_u64 v[206:207], s[14:15], 0, v[166:167]
	s_mov_b32 m0, vcc_lo
	s_nop 0
	global_load_lds_dwordx4 v[206:207], off
	s_barrier
	s_waitcnt lgkmcnt(0)
	s_setprio 1
	s_waitcnt lgkmcnt(0)
	v_mfma_scale_f32_16x16x128_f8f6f4 v[152:155], v[26:33], v[182:189], 0, v176, v1 op_sel_hi:[0,0,0]
	v_mfma_scale_f32_16x16x128_f8f6f4 v[148:151], v[18:25], v[182:189], 0, v176, v1 op_sel_hi:[0,0,0]
	v_mfma_scale_f32_16x16x128_f8f6f4 v[136:139], v[26:33], v[190:197], 0, v176, v1 op_sel_hi:[0,0,0]
	v_mfma_scale_f32_16x16x128_f8f6f4 v[132:135], v[18:25], v[190:197], 0, v176, v1 op_sel_hi:[0,0,0]
	v_mfma_scale_f32_16x16x128_f8f6f4 v[120:123], v[26:33], v[198:205], 0, v176, v1 op_sel_hi:[0,0,0]
	v_mfma_scale_f32_16x16x128_f8f6f4 v[116:119], v[18:25], v[198:205], 0, v176, v1 op_sel_hi:[0,0,0]
	v_mfma_scale_f32_16x16x128_f8f6f4 v[104:107], v[26:33], v[218:225], 0, v176, v1 op_sel_hi:[0,0,0]
	v_mfma_scale_f32_16x16x128_f8f6f4 v[100:103], v[18:25], v[218:225], 0, v176, v1 op_sel_hi:[0,0,0]
	s_setprio 0
	s_mov_b64 s[14:15], s[54:55]
	s_mov_b32 m0, s41
	s_barrier
	ds_read_b128 v[182:185], v180 offset:16384
	ds_read_b128 v[186:189], v180 offset:17408
	ds_read_b128 v[190:193], v180 offset:18432
	ds_read_b128 v[194:197], v180 offset:19456
	ds_read_b128 v[198:201], v180 offset:20480
	ds_read_b128 v[202:205], v180 offset:21504
	ds_read_b128 v[218:221], v180 offset:22528
	ds_read_b128 v[222:225], v180 offset:23552
	s_nop 0
	v_lshl_add_u64 v[206:207], s[14:15], 0, v[168:169]
	global_load_lds_dwordx4 v[206:207], off
	v_lshl_add_u64 v[206:207], s[14:15], 0, v[170:171]
	s_mov_b32 m0, s77
	s_nop 0
	global_load_lds_dwordx4 v[206:207], off
	s_barrier
	s_waitcnt lgkmcnt(0)
	s_setprio 1
	s_waitcnt lgkmcnt(0)
	v_mfma_scale_f32_16x16x128_f8f6f4 v[96:99], v[10:17], v[182:189], 0, v35, v1 op_sel_hi:[0,0,0]
	v_mfma_scale_f32_16x16x128_f8f6f4 v[92:95], v[2:9], v[182:189], 0, v35, v1 op_sel_hi:[0,0,0]
	v_mfma_scale_f32_16x16x128_f8f6f4 v[80:83], v[10:17], v[190:197], 0, v35, v1 op_sel_hi:[0,0,0]
	v_mfma_scale_f32_16x16x128_f8f6f4 v[76:79], v[2:9], v[190:197], 0, v35, v1 op_sel_hi:[0,0,0]
	v_mfma_scale_f32_16x16x128_f8f6f4 v[64:67], v[10:17], v[198:205], 0, v35, v1 op_sel_hi:[0,0,0]
	v_mfma_scale_f32_16x16x128_f8f6f4 v[60:63], v[2:9], v[198:205], 0, v35, v1 op_sel_hi:[0,0,0]
	v_mfma_scale_f32_16x16x128_f8f6f4 v[48:51], v[10:17], v[218:225], 0, v35, v1 op_sel_hi:[0,0,0]
	v_mfma_scale_f32_16x16x128_f8f6f4 v[44:47], v[2:9], v[218:225], 0, v35, v1 op_sel_hi:[0,0,0]
	s_setprio 0
	s_barrier
	s_mov_b32 m0, s89
	s_nop 0
	v_lshl_add_u64 v[2:3], s[56:57], 0, v[164:165]
	global_load_lds_dwordx4 v[2:3], off
	v_lshl_add_u64 v[2:3], s[56:57], 0, v[166:167]
	s_mov_b32 m0, s88
	s_nop 0
	global_load_lds_dwordx4 v[2:3], off
	s_waitcnt vmcnt(6)
	s_barrier
	s_setprio 1
	v_mfma_scale_f32_16x16x128_f8f6f4 v[88:91], v[26:33], v[182:189], 0, v176, v1 op_sel_hi:[0,0,0]
	v_mfma_scale_f32_16x16x128_f8f6f4 v[84:87], v[18:25], v[182:189], 0, v176, v1 op_sel_hi:[0,0,0]
	v_mfma_scale_f32_16x16x128_f8f6f4 v[72:75], v[26:33], v[190:197], 0, v176, v1 op_sel_hi:[0,0,0]
	v_mfma_scale_f32_16x16x128_f8f6f4 v[68:71], v[18:25], v[190:197], 0, v176, v1 op_sel_hi:[0,0,0]
	v_mfma_scale_f32_16x16x128_f8f6f4 v[56:59], v[26:33], v[198:205], 0, v176, v1 op_sel_hi:[0,0,0]
	v_mfma_scale_f32_16x16x128_f8f6f4 v[52:55], v[18:25], v[198:205], 0, v176, v1 op_sel_hi:[0,0,0]
	v_mfma_scale_f32_16x16x128_f8f6f4 v[40:43], v[26:33], v[218:225], 0, v176, v1 op_sel_hi:[0,0,0]
	v_mfma_scale_f32_16x16x128_f8f6f4 v[36:39], v[18:25], v[218:225], 0, v176, v1 op_sel_hi:[0,0,0]
	s_setprio 0
	v_add_u32_e32 v6, s87, v178
	s_barrier
	ds_read_b128 v[10:13], v6
	ds_read_b128 v[14:17], v6 offset:1024
	ds_read_b128 v[2:5], v6 offset:2048
	ds_read_b128 v[6:9], v6 offset:3072
	s_mov_b32 m0, s78
	ds_read_b128 v[18:21], v180 offset:32768
	ds_read_b128 v[22:25], v180 offset:33792
	ds_read_b128 v[26:29], v180 offset:34816
	ds_read_b128 v[30:33], v180 offset:35840
	ds_read_b128 v[182:185], v180 offset:36864
	ds_read_b128 v[186:189], v180 offset:37888
	ds_read_b128 v[190:193], v180 offset:38912
	ds_read_b128 v[194:197], v180 offset:39936
	s_nop 0
	v_lshl_add_u64 v[198:199], s[54:55], 0, v[172:173]
	global_load_lds_dwordx4 v[198:199], off
	v_lshl_add_u64 v[198:199], s[54:55], 0, v[174:175]
	s_mov_b32 m0, s79
	s_nop 0
	global_load_lds_dwordx4 v[198:199], off
	s_waitcnt lgkmcnt(8)
	s_barrier
	s_waitcnt lgkmcnt(0)
	s_setprio 1
	s_waitcnt lgkmcnt(0)
	v_mfma_scale_f32_16x16x128_f8f6f4 v[160:163], v[10:17], v[18:25], v[160:163], v35, v1 op_sel_hi:[0,0,0]
	v_mfma_scale_f32_16x16x128_f8f6f4 v[156:159], v[2:9], v[18:25], v[156:159], v35, v1 op_sel_hi:[0,0,0]
	v_mfma_scale_f32_16x16x128_f8f6f4 v[144:147], v[10:17], v[26:33], v[144:147], v35, v1 op_sel_hi:[0,0,0]
	v_mfma_scale_f32_16x16x128_f8f6f4 v[140:143], v[2:9], v[26:33], v[140:143], v35, v1 op_sel_hi:[0,0,0]
	v_mfma_scale_f32_16x16x128_f8f6f4 v[128:131], v[10:17], v[182:189], v[128:131], v35, v1 op_sel_hi:[0,0,0]
	v_mfma_scale_f32_16x16x128_f8f6f4 v[124:127], v[2:9], v[182:189], v[124:127], v35, v1 op_sel_hi:[0,0,0]
	v_mfma_scale_f32_16x16x128_f8f6f4 v[112:115], v[10:17], v[190:197], v[112:115], v35, v1 op_sel_hi:[0,0,0]
	v_mfma_scale_f32_16x16x128_f8f6f4 v[108:111], v[2:9], v[190:197], v[108:111], v35, v1 op_sel_hi:[0,0,0]
	s_setprio 0
	s_barrier
	v_add_u32_e32 v181, s85, v178
	s_mov_b32 m0, s86
	ds_read_b128 v[198:201], v181
	ds_read_b128 v[202:205], v181 offset:1024
	ds_read_b128 v[218:221], v181 offset:2048
	ds_read_b128 v[222:225], v181 offset:3072
	s_nop 0
	v_lshl_add_u64 v[206:207], s[52:53], 0, v[164:165]
	global_load_lds_dwordx4 v[206:207], off
	v_lshl_add_u64 v[206:207], s[52:53], 0, v[166:167]
	s_mov_b32 m0, s19
	s_nop 0
	global_load_lds_dwordx4 v[206:207], off
	s_barrier
	s_waitcnt lgkmcnt(0)
	s_setprio 1
	s_waitcnt lgkmcnt(0)
	v_mfma_scale_f32_16x16x128_f8f6f4 v[152:155], v[198:205], v[18:25], v[152:155], v176, v1 op_sel_hi:[0,0,0]
	v_mfma_scale_f32_16x16x128_f8f6f4 v[148:151], v[218:225], v[18:25], v[148:151], v176, v1 op_sel_hi:[0,0,0]
	v_mfma_scale_f32_16x16x128_f8f6f4 v[136:139], v[198:205], v[26:33], v[136:139], v176, v1 op_sel_hi:[0,0,0]
	v_mfma_scale_f32_16x16x128_f8f6f4 v[132:135], v[218:225], v[26:33], v[132:135], v176, v1 op_sel_hi:[0,0,0]
	v_mfma_scale_f32_16x16x128_f8f6f4 v[120:123], v[198:205], v[182:189], v[120:123], v176, v1 op_sel_hi:[0,0,0]
	v_mfma_scale_f32_16x16x128_f8f6f4 v[116:119], v[218:225], v[182:189], v[116:119], v176, v1 op_sel_hi:[0,0,0]
	v_mfma_scale_f32_16x16x128_f8f6f4 v[104:107], v[198:205], v[190:197], v[104:107], v176, v1 op_sel_hi:[0,0,0]
	v_mfma_scale_f32_16x16x128_f8f6f4 v[100:103], v[218:225], v[190:197], v[100:103], v176, v1 op_sel_hi:[0,0,0]
	s_setprio 0
	s_mov_b32 m0, s80
	s_barrier
	ds_read_b128 v[18:21], v180 offset:49152
	ds_read_b128 v[22:25], v180 offset:50176
	ds_read_b128 v[26:29], v180 offset:51200
	ds_read_b128 v[30:33], v180 offset:52224
	ds_read_b128 v[182:185], v180 offset:53248
	ds_read_b128 v[186:189], v180 offset:54272
	ds_read_b128 v[190:193], v180 offset:55296
	ds_read_b128 v[194:197], v180 offset:56320
	s_nop 0
	v_lshl_add_u64 v[206:207], s[50:51], 0, v[168:169]
	global_load_lds_dwordx4 v[206:207], off
	v_lshl_add_u64 v[206:207], s[50:51], 0, v[170:171]
	s_mov_b32 m0, s81
	s_nop 0
	global_load_lds_dwordx4 v[206:207], off
	s_barrier
	s_waitcnt lgkmcnt(0)
	s_setprio 1
	s_waitcnt lgkmcnt(0)
	v_mfma_scale_f32_16x16x128_f8f6f4 v[96:99], v[10:17], v[18:25], v[96:99], v35, v1 op_sel_hi:[0,0,0]
	v_mfma_scale_f32_16x16x128_f8f6f4 v[92:95], v[2:9], v[18:25], v[92:95], v35, v1 op_sel_hi:[0,0,0]
	v_mfma_scale_f32_16x16x128_f8f6f4 v[80:83], v[10:17], v[26:33], v[80:83], v35, v1 op_sel_hi:[0,0,0]
	v_mfma_scale_f32_16x16x128_f8f6f4 v[76:79], v[2:9], v[26:33], v[76:79], v35, v1 op_sel_hi:[0,0,0]
	v_mfma_scale_f32_16x16x128_f8f6f4 v[64:67], v[10:17], v[182:189], v[64:67], v35, v1 op_sel_hi:[0,0,0]
	v_mfma_scale_f32_16x16x128_f8f6f4 v[60:63], v[2:9], v[182:189], v[60:63], v35, v1 op_sel_hi:[0,0,0]
	v_mfma_scale_f32_16x16x128_f8f6f4 v[48:51], v[10:17], v[190:197], v[48:51], v35, v1 op_sel_hi:[0,0,0]
	v_mfma_scale_f32_16x16x128_f8f6f4 v[44:47], v[2:9], v[190:197], v[44:47], v35, v1 op_sel_hi:[0,0,0]
	s_setprio 0
	s_barrier
	s_mov_b32 m0, s1
	s_nop 0
	v_lshl_add_u64 v[2:3], s[48:49], 0, v[164:165]
	global_load_lds_dwordx4 v[2:3], off
	v_lshl_add_u64 v[2:3], s[48:49], 0, v[166:167]
	s_mov_b32 m0, s0
	s_nop 0
	global_load_lds_dwordx4 v[2:3], off
	s_waitcnt vmcnt(6)
	s_barrier
	s_setprio 1
	v_mfma_scale_f32_16x16x128_f8f6f4 v[88:91], v[198:205], v[18:25], v[88:91], v176, v1 op_sel_hi:[0,0,0]
	v_mfma_scale_f32_16x16x128_f8f6f4 v[84:87], v[218:225], v[18:25], v[84:87], v176, v1 op_sel_hi:[0,0,0]
	v_mfma_scale_f32_16x16x128_f8f6f4 v[72:75], v[198:205], v[26:33], v[72:75], v176, v1 op_sel_hi:[0,0,0]
	v_mfma_scale_f32_16x16x128_f8f6f4 v[68:71], v[218:225], v[26:33], v[68:71], v176, v1 op_sel_hi:[0,0,0]
	v_mfma_scale_f32_16x16x128_f8f6f4 v[56:59], v[198:205], v[182:189], v[56:59], v176, v1 op_sel_hi:[0,0,0]
	v_mfma_scale_f32_16x16x128_f8f6f4 v[52:55], v[218:225], v[182:189], v[52:55], v176, v1 op_sel_hi:[0,0,0]
	v_mfma_scale_f32_16x16x128_f8f6f4 v[40:43], v[198:205], v[190:197], v[40:43], v176, v1 op_sel_hi:[0,0,0]
	v_mfma_scale_f32_16x16x128_f8f6f4 v[36:39], v[218:225], v[190:197], v[36:39], v176, v1 op_sel_hi:[0,0,0]
	s_setprio 0
	s_movk_i32 s0, 0x100
	s_andn2_b64 vcc, exec, s[46:47]
	s_mov_b64 s[48:49], -1
	s_mov_b64 s[46:47], 0
	s_barrier
	s_cbranch_vccz .LBB0_1339
	s_branch .Lpeel_exit_3

.Lpeel_exit_3:
	v_med3_f32 v5, v160, s75, v238
	v_med3_f32 v6, v161, s75, v238
	v_mov_b32_e32 v4, v34
	v_cvt_pk_fp8_f32 v4, v5, v6
	v_med3_f32 v7, v162, s75, v238
	v_med3_f32 v10, v163, s75, v238
	v_med3_f32 v6, v156, s75, v238
	v_cvt_pk_fp8_f32 v4, v7, v10 op_sel:[0,0,1]
	v_med3_f32 v7, v157, s75, v238
	v_mov_b32_e32 v5, v34
	v_cvt_pk_fp8_f32 v5, v6, v7
	v_med3_f32 v10, v158, s75, v238
	v_med3_f32 v11, v159, s75, v238
	v_med3_f32 v7, v152, s75, v238
	v_cvt_pk_fp8_f32 v5, v10, v11 op_sel:[0,0,1]
	v_med3_f32 v10, v153, s75, v238
	v_mov_b32_e32 v6, v34
	v_cvt_pk_fp8_f32 v6, v7, v10
	v_med3_f32 v11, v154, s75, v238
	v_med3_f32 v12, v155, s75, v238
	v_med3_f32 v10, v148, s75, v238
	v_cvt_pk_fp8_f32 v6, v11, v12 op_sel:[0,0,1]
	v_med3_f32 v11, v149, s75, v238
	v_mov_b32_e32 v7, v34
	v_cvt_pk_fp8_f32 v7, v10, v11
	s_nop 7
	s_nop 7
	s_nop 3
	s_mov_b32 s0, 0
	s_lshl_b32 s1, s40, 8
	s_add_i32 s0, s0, s1
	v_add_u32_e32 v2, s0, v177
	v_med3_f32 v12, v150, s75, v238
	v_med3_f32 v13, v151, s75, v238
	v_ashrrev_i32_e32 v3, 31, v2
	v_cvt_pk_fp8_f32 v7, v12, v13 op_sel:[0,0,1]
	v_lshl_or_b32 v8, s84, 8, v179
	v_lshlrev_b64 v[2:3], 10, v[2:3]
	v_ashrrev_i32_e32 v9, 31, v8
	v_lshl_add_u64 v[2:3], s[16:17], 0, v[2:3]
	v_lshl_add_u64 v[2:3], v[2:3], 0, v[8:9]
	global_store_dwordx4 v[2:3], v[4:7], off
	v_med3_f32 v8, v147, s75, v238
	v_med3_f32 v9, v143, s75, v238
	v_med3_f32 v5, v144, s75, v238
	v_med3_f32 v6, v145, s75, v238
	v_mov_b32_e32 v4, v34
	v_cvt_pk_fp8_f32 v4, v5, v6
	v_med3_f32 v7, v146, s75, v238
	v_med3_f32 v6, v140, s75, v238
	v_mov_b32_e32 v5, v34
	v_cvt_pk_fp8_f32 v4, v7, v8 op_sel:[0,0,1]
	v_med3_f32 v7, v141, s75, v238
	v_cvt_pk_fp8_f32 v5, v6, v7
	v_med3_f32 v8, v142, s75, v238
	v_med3_f32 v7, v136, s75, v238
	v_mov_b32_e32 v6, v34
	v_cvt_pk_fp8_f32 v5, v8, v9 op_sel:[0,0,1]
	v_med3_f32 v8, v137, s75, v238
	v_cvt_pk_fp8_f32 v6, v7, v8
	v_med3_f32 v9, v138, s75, v238
	v_med3_f32 v10, v139, s75, v238
	v_med3_f32 v8, v132, s75, v238
	v_cvt_pk_fp8_f32 v6, v9, v10 op_sel:[0,0,1]
	v_med3_f32 v9, v133, s75, v238
	v_mov_b32_e32 v7, v34
	v_cvt_pk_fp8_f32 v7, v8, v9
	v_med3_f32 v10, v134, s75, v238
	v_med3_f32 v11, v135, s75, v238
	s_movk_i32 s92, 0x4000
	v_cvt_pk_fp8_f32 v7, v10, v11 op_sel:[0,0,1]
	v_add_co_u32_e32 v8, vcc, s92, v2
	v_med3_f32 v10, v123, s75, v238
	s_nop 0
	v_addc_co_u32_e32 v9, vcc, 0, v3, vcc
	global_store_dwordx4 v[8:9], v[4:7], off
	v_med3_f32 v8, v131, s75, v238
	v_med3_f32 v9, v127, s75, v238
	v_med3_f32 v5, v128, s75, v238
	v_med3_f32 v6, v129, s75, v238
	v_mov_b32_e32 v4, v34
	v_cvt_pk_fp8_f32 v4, v5, v6
	v_med3_f32 v7, v130, s75, v238
	v_med3_f32 v6, v124, s75, v238
	v_mov_b32_e32 v5, v34
	v_cvt_pk_fp8_f32 v4, v7, v8 op_sel:[0,0,1]
	v_med3_f32 v7, v125, s75, v238
	v_cvt_pk_fp8_f32 v5, v6, v7
	v_med3_f32 v8, v126, s75, v238
	v_med3_f32 v7, v120, s75, v238
	v_mov_b32_e32 v6, v34
	v_cvt_pk_fp8_f32 v5, v8, v9 op_sel:[0,0,1]
	v_med3_f32 v8, v121, s75, v238
	v_cvt_pk_fp8_f32 v6, v7, v8
	v_med3_f32 v9, v122, s75, v238
	v_med3_f32 v8, v116, s75, v238
	v_mov_b32_e32 v7, v34
	v_cvt_pk_fp8_f32 v6, v9, v10 op_sel:[0,0,1]
	v_med3_f32 v9, v117, s75, v238
	v_cvt_pk_fp8_f32 v7, v8, v9
	v_med3_f32 v10, v118, s75, v238
	v_med3_f32 v11, v119, s75, v238
	s_mov_b32 s0, 0x8000
	v_cvt_pk_fp8_f32 v7, v10, v11 op_sel:[0,0,1]
	v_add_co_u32_e32 v8, vcc, s0, v2
	v_med3_f32 v10, v107, s75, v238
	s_nop 0
	v_addc_co_u32_e32 v9, vcc, 0, v3, vcc
	global_store_dwordx4 v[8:9], v[4:7], off
	v_med3_f32 v8, v115, s75, v238
	v_med3_f32 v9, v111, s75, v238
	v_med3_f32 v5, v112, s75, v238
	v_med3_f32 v6, v113, s75, v238
	v_mov_b32_e32 v4, v34
	v_cvt_pk_fp8_f32 v4, v5, v6
	v_med3_f32 v7, v114, s75, v238
	v_med3_f32 v6, v108, s75, v238
	v_mov_b32_e32 v5, v34
	v_cvt_pk_fp8_f32 v4, v7, v8 op_sel:[0,0,1]
	v_med3_f32 v7, v109, s75, v238
	v_cvt_pk_fp8_f32 v5, v6, v7
	v_med3_f32 v8, v110, s75, v238
	v_med3_f32 v7, v104, s75, v238
	v_mov_b32_e32 v6, v34
	v_cvt_pk_fp8_f32 v5, v8, v9 op_sel:[0,0,1]
	v_med3_f32 v8, v105, s75, v238
	v_cvt_pk_fp8_f32 v6, v7, v8
	v_med3_f32 v9, v106, s75, v238
	v_med3_f32 v8, v100, s75, v238
	v_mov_b32_e32 v7, v34
	v_cvt_pk_fp8_f32 v6, v9, v10 op_sel:[0,0,1]
	v_med3_f32 v9, v101, s75, v238
	v_cvt_pk_fp8_f32 v7, v8, v9
	v_med3_f32 v10, v102, s75, v238
	v_med3_f32 v11, v103, s75, v238
	s_mov_b32 s0, 0xc000
	v_cvt_pk_fp8_f32 v7, v10, v11 op_sel:[0,0,1]
	v_add_co_u32_e32 v8, vcc, s0, v2
	v_med3_f32 v10, v91, s75, v238
	s_nop 0
	v_addc_co_u32_e32 v9, vcc, 0, v3, vcc
	global_store_dwordx4 v[8:9], v[4:7], off
	v_med3_f32 v8, v99, s75, v238
	v_med3_f32 v9, v95, s75, v238
	v_med3_f32 v5, v96, s75, v238
	v_med3_f32 v6, v97, s75, v238
	v_mov_b32_e32 v4, v34
	v_cvt_pk_fp8_f32 v4, v5, v6
	v_med3_f32 v7, v98, s75, v238
	v_med3_f32 v6, v92, s75, v238
	v_mov_b32_e32 v5, v34
	v_cvt_pk_fp8_f32 v4, v7, v8 op_sel:[0,0,1]
	v_med3_f32 v7, v93, s75, v238
	v_cvt_pk_fp8_f32 v5, v6, v7
	v_med3_f32 v8, v94, s75, v238
	v_med3_f32 v7, v88, s75, v238
	v_mov_b32_e32 v6, v34
	v_cvt_pk_fp8_f32 v5, v8, v9 op_sel:[0,0,1]
	v_med3_f32 v8, v89, s75, v238
	v_cvt_pk_fp8_f32 v6, v7, v8
	v_med3_f32 v9, v90, s75, v238
	v_med3_f32 v8, v84, s75, v238
	v_mov_b32_e32 v7, v34
	v_cvt_pk_fp8_f32 v6, v9, v10 op_sel:[0,0,1]
	v_med3_f32 v9, v85, s75, v238
	v_cvt_pk_fp8_f32 v7, v8, v9
	v_med3_f32 v10, v86, s75, v238
	v_med3_f32 v11, v87, s75, v238
	s_mov_b32 s0, 0x20000
	v_cvt_pk_fp8_f32 v7, v10, v11 op_sel:[0,0,1]
	v_add_co_u32_e32 v8, vcc, s0, v2
	v_med3_f32 v10, v75, s75, v238
	s_nop 0
	v_addc_co_u32_e32 v9, vcc, 0, v3, vcc
	global_store_dwordx4 v[8:9], v[4:7], off
	v_med3_f32 v8, v83, s75, v238
	v_med3_f32 v9, v79, s75, v238
	v_med3_f32 v5, v80, s75, v238
	v_med3_f32 v6, v81, s75, v238
	v_mov_b32_e32 v4, v34
	v_cvt_pk_fp8_f32 v4, v5, v6
	v_med3_f32 v7, v82, s75, v238
	v_med3_f32 v6, v76, s75, v238
	v_mov_b32_e32 v5, v34
	v_cvt_pk_fp8_f32 v4, v7, v8 op_sel:[0,0,1]
	v_med3_f32 v7, v77, s75, v238
	v_cvt_pk_fp8_f32 v5, v6, v7
	v_med3_f32 v8, v78, s75, v238
	v_med3_f32 v7, v72, s75, v238
	v_mov_b32_e32 v6, v34
	v_cvt_pk_fp8_f32 v5, v8, v9 op_sel:[0,0,1]
	v_med3_f32 v8, v73, s75, v238
	v_cvt_pk_fp8_f32 v6, v7, v8
	v_med3_f32 v9, v74, s75, v238
	v_med3_f32 v8, v68, s75, v238
	v_mov_b32_e32 v7, v34
	v_cvt_pk_fp8_f32 v6, v9, v10 op_sel:[0,0,1]
	v_med3_f32 v9, v69, s75, v238
	v_cvt_pk_fp8_f32 v7, v8, v9
	v_med3_f32 v10, v70, s75, v238
	v_med3_f32 v11, v71, s75, v238
	s_mov_b32 s0, 0x24000
	v_cvt_pk_fp8_f32 v7, v10, v11 op_sel:[0,0,1]
	v_add_co_u32_e32 v8, vcc, s0, v2
	v_med3_f32 v10, v59, s75, v238
	s_nop 0
	v_addc_co_u32_e32 v9, vcc, 0, v3, vcc
	global_store_dwordx4 v[8:9], v[4:7], off
	v_med3_f32 v8, v67, s75, v238
	v_med3_f32 v9, v63, s75, v238
	v_med3_f32 v5, v64, s75, v238
	v_med3_f32 v6, v65, s75, v238
	v_mov_b32_e32 v4, v34
	v_cvt_pk_fp8_f32 v4, v5, v6
	v_med3_f32 v7, v66, s75, v238
	v_med3_f32 v6, v60, s75, v238
	v_mov_b32_e32 v5, v34
	v_cvt_pk_fp8_f32 v4, v7, v8 op_sel:[0,0,1]
	v_med3_f32 v7, v61, s75, v238
	v_cvt_pk_fp8_f32 v5, v6, v7
	v_med3_f32 v8, v62, s75, v238
	v_med3_f32 v7, v56, s75, v238
	v_mov_b32_e32 v6, v34
	v_cvt_pk_fp8_f32 v5, v8, v9 op_sel:[0,0,1]
	v_med3_f32 v8, v57, s75, v238
	v_cvt_pk_fp8_f32 v6, v7, v8
	v_med3_f32 v9, v58, s75, v238
	v_med3_f32 v8, v52, s75, v238
	v_mov_b32_e32 v7, v34
	v_cvt_pk_fp8_f32 v6, v9, v10 op_sel:[0,0,1]
	v_med3_f32 v9, v53, s75, v238
	v_cvt_pk_fp8_f32 v7, v8, v9
	v_med3_f32 v10, v54, s75, v238
	v_med3_f32 v11, v55, s75, v238
	s_mov_b32 s0, 0x28000
	v_cvt_pk_fp8_f32 v7, v10, v11 op_sel:[0,0,1]
	v_add_co_u32_e32 v8, vcc, s0, v2
	v_med3_f32 v10, v43, s75, v238
	s_nop 0
	v_addc_co_u32_e32 v9, vcc, 0, v3, vcc
	global_store_dwordx4 v[8:9], v[4:7], off
	v_med3_f32 v8, v51, s75, v238
	v_med3_f32 v9, v47, s75, v238
	v_med3_f32 v5, v48, s75, v238
	v_med3_f32 v6, v49, s75, v238
	v_mov_b32_e32 v4, v34
	v_cvt_pk_fp8_f32 v4, v5, v6
	v_med3_f32 v7, v50, s75, v238
	v_med3_f32 v6, v44, s75, v238
	v_mov_b32_e32 v5, v34
	v_cvt_pk_fp8_f32 v4, v7, v8 op_sel:[0,0,1]
	v_med3_f32 v7, v45, s75, v238
	v_cvt_pk_fp8_f32 v5, v6, v7
	v_med3_f32 v8, v46, s75, v238
	v_med3_f32 v7, v40, s75, v238
	v_mov_b32_e32 v6, v34
	v_cvt_pk_fp8_f32 v5, v8, v9 op_sel:[0,0,1]
	v_med3_f32 v8, v41, s75, v238
	v_cvt_pk_fp8_f32 v6, v7, v8
	v_med3_f32 v9, v42, s75, v238
	v_med3_f32 v8, v36, s75, v238
	v_mov_b32_e32 v7, v34
	v_cvt_pk_fp8_f32 v6, v9, v10 op_sel:[0,0,1]
	v_med3_f32 v9, v37, s75, v238
	v_cvt_pk_fp8_f32 v7, v8, v9
	v_med3_f32 v10, v38, s75, v238
	v_med3_f32 v11, v39, s75, v238
	v_add_co_u32_e32 v2, vcc, 0x2c000, v2
	v_cvt_pk_fp8_f32 v7, v10, v11 op_sel:[0,0,1]
	s_nop 0
	v_addc_co_u32_e32 v3, vcc, 0, v3, vcc
	s_and_b64 vcc, exec, s[38:39]
	s_mov_b32 s84, s83
	s_mov_b32 s40, s18
	s_mov_b64 s[44:45], s[36:37]
	s_mov_b64 s[42:43], s[28:29]
	s_movk_i32 s93, 0x800
	global_store_dwordx4 v[2:3], v[4:7], off
	s_cbranch_vccz .LBB0_1332
	s_waitcnt vmcnt(0)
	s_cmpk_gt_u32 s13, 0xff
	s_cbranch_scc1 .LBB0_1343
	s_barrier
